# wave/16-lane sum reductions: ds_swizzle SWAP 1/2/4/8 LDS round trips replaced by v_mov_b32_dpp (quad_perm, row_half_mirror, row_mirror); rowpass, prep, route1, scan finish
# speedup vs baseline: 1.0025x; 1.0025x over previous
.LBB0_140:
	v_cvt_pk_f32_fp8_sdwa v[52:53], v100 src0_sel:WORD_1
	v_cvt_pk_f32_fp8_e32 v[54:55], v100
	v_cvt_pk_f32_fp8_sdwa v[102:103], v101 src0_sel:WORD_1
	v_cvt_pk_f32_fp8_e32 v[104:105], v98
	v_cvt_pk_f32_fp8_sdwa v[106:107], v98 src0_sel:WORD_1
	v_cvt_pk_f32_fp8_e32 v[108:109], v99
	v_cvt_pk_f32_fp8_sdwa v[98:99], v99 src0_sel:WORD_1
	v_cvt_pk_f32_fp8_e32 v[100:101], v101
	v_pk_add_f32 v[52:53], v[52:53], 0 op_sel_hi:[1,0]
	v_pk_add_f32 v[54:55], v[54:55], 0 op_sel_hi:[1,0]
	v_pk_add_f32 v[102:103], v[102:103], 0 op_sel_hi:[1,0]
	v_pk_add_f32 v[54:55], v[54:55], v[104:105]
	v_pk_add_f32 v[52:53], v[52:53], v[106:107]
	v_pk_add_f32 v[98:99], v[102:103], v[98:99]
	v_cvt_pk_f32_fp8_sdwa v[102:103], v96 src0_sel:WORD_1
	v_cvt_pk_f32_fp8_e32 v[104:105], v96
	v_cvt_pk_f32_fp8_sdwa v[106:107], v97 src0_sel:WORD_1
	v_cvt_pk_f32_fp8_e32 v[96:97], v97
	v_pk_add_f32 v[100:101], v[100:101], 0 op_sel_hi:[1,0]
	v_pk_add_f32 v[52:53], v[52:53], v[102:103]
	v_pk_add_f32 v[100:101], v[100:101], v[108:109]
	v_pk_add_f32 v[54:55], v[54:55], v[104:105]
	v_pk_add_f32 v[96:97], v[100:101], v[96:97]
	v_cvt_pk_f32_fp8_e32 v[100:101], v94
	v_cvt_pk_f32_fp8_sdwa v[102:103], v94 src0_sel:WORD_1
	v_cvt_pk_f32_fp8_e32 v[104:105], v95
	v_cvt_pk_f32_fp8_sdwa v[94:95], v95 src0_sel:WORD_1
	v_pk_add_f32 v[98:99], v[98:99], v[106:107]
	v_pk_add_f32 v[54:55], v[54:55], v[100:101]
	v_pk_add_f32 v[52:53], v[52:53], v[102:103]
	v_pk_add_f32 v[96:97], v[96:97], v[104:105]
	v_pk_add_f32 v[94:95], v[98:99], v[94:95]
	v_lshlrev_b32_e32 v98, 16, v36
	v_and_b32_e32 v99, 0xffff0000, v36
	v_lshlrev_b32_e32 v36, 16, v37
	v_and_b32_e32 v37, 0xffff0000, v37
	v_lshlrev_b32_e32 v100, 16, v38
	v_and_b32_e32 v101, 0xffff0000, v38
	v_lshlrev_b32_e32 v38, 16, v39
	v_and_b32_e32 v39, 0xffff0000, v39
	v_pk_fma_f32 v[36:37], v[2:3], v[52:53], v[36:37]
	v_pk_fma_f32 v[52:53], v[0:1], v[54:55], v[98:99]
	v_pk_fma_f32 v[38:39], v[6:7], v[94:95], v[38:39]
	v_pk_fma_f32 v[54:55], v[4:5], v[96:97], v[100:101]
	v_cvt_pk_f32_fp8_sdwa v[94:95], v92 src0_sel:WORD_1
	v_cvt_pk_f32_fp8_e32 v[96:97], v92
	v_cvt_pk_f32_fp8_sdwa v[98:99], v93 src0_sel:WORD_1
	v_cvt_pk_f32_fp8_e32 v[100:101], v86
	v_cvt_pk_f32_fp8_sdwa v[102:103], v86 src0_sel:WORD_1
	v_cvt_pk_f32_fp8_e32 v[104:105], v87
	v_cvt_pk_f32_fp8_sdwa v[86:87], v87 src0_sel:WORD_1
	v_cvt_pk_f32_fp8_e32 v[92:93], v93
	v_pk_add_f32 v[94:95], v[94:95], 0 op_sel_hi:[1,0]
	v_pk_add_f32 v[96:97], v[96:97], 0 op_sel_hi:[1,0]
	v_pk_add_f32 v[98:99], v[98:99], 0 op_sel_hi:[1,0]
	v_pk_add_f32 v[96:97], v[96:97], v[100:101]
	v_pk_add_f32 v[94:95], v[94:95], v[102:103]
	v_pk_add_f32 v[86:87], v[98:99], v[86:87]
	v_cvt_pk_f32_fp8_sdwa v[98:99], v58 src0_sel:WORD_1
	v_cvt_pk_f32_fp8_e32 v[100:101], v58
	v_cvt_pk_f32_fp8_sdwa v[102:103], v59 src0_sel:WORD_1
	v_cvt_pk_f32_fp8_e32 v[58:59], v59
	v_pk_add_f32 v[92:93], v[92:93], 0 op_sel_hi:[1,0]
	v_pk_add_f32 v[94:95], v[94:95], v[98:99]
	v_pk_add_f32 v[92:93], v[92:93], v[104:105]
	v_pk_add_f32 v[96:97], v[96:97], v[100:101]
	v_pk_add_f32 v[58:59], v[92:93], v[58:59]
	v_cvt_pk_f32_fp8_e32 v[92:93], v56
	v_cvt_pk_f32_fp8_sdwa v[98:99], v56 src0_sel:WORD_1
	v_cvt_pk_f32_fp8_e32 v[100:101], v57
	v_cvt_pk_f32_fp8_sdwa v[56:57], v57 src0_sel:WORD_1
	v_pk_add_f32 v[86:87], v[86:87], v[102:103]
	v_pk_add_f32 v[94:95], v[94:95], v[98:99]
	v_pk_add_f32 v[92:93], v[96:97], v[92:93]
	v_pk_add_f32 v[56:57], v[86:87], v[56:57]
	v_lshlrev_b32_e32 v86, 16, v32
	v_and_b32_e32 v87, 0xffff0000, v32
	v_lshlrev_b32_e32 v32, 16, v33
	v_and_b32_e32 v33, 0xffff0000, v33
	v_pk_fma_f32 v[94:95], v[18:19], v[94:95], v[32:33]
	v_mul_f32_e32 v32, v53, v53
	v_mul_f32_e32 v33, v37, v37
	v_lshlrev_b32_e32 v96, 16, v34
	v_and_b32_e32 v97, 0xffff0000, v34
	v_lshlrev_b32_e32 v34, 16, v35
	v_and_b32_e32 v35, 0xffff0000, v35
	v_fmac_f32_e32 v32, v52, v52
	v_fmac_f32_e32 v33, v36, v36
	v_pk_fma_f32 v[56:57], v[22:23], v[56:57], v[34:35]
	v_add_f32_e32 v32, v32, v33
	v_mul_f32_e32 v33, v55, v55
	v_mul_f32_e32 v34, v39, v39
	v_fmac_f32_e32 v33, v54, v54
	v_fmac_f32_e32 v34, v38, v38
	v_pk_fma_f32 v[86:87], v[16:17], v[92:93], v[86:87]
	v_add_f32_e32 v33, v33, v34
	v_add_f32_e32 v32, v32, v33
	v_mul_f32_e32 v33, v87, v87
	v_mul_f32_e32 v34, v95, v95
	v_pk_add_f32 v[58:59], v[58:59], v[100:101]
	v_fmac_f32_e32 v33, v86, v86
	v_fmac_f32_e32 v34, v94, v94
	v_pk_fma_f32 v[58:59], v[20:21], v[58:59], v[96:97]
	v_add_f32_e32 v33, v33, v34
	v_add_f32_e32 v32, v32, v33
	v_mul_f32_e32 v33, v59, v59
	v_mul_f32_e32 v34, v57, v57
	v_fmac_f32_e32 v33, v58, v58
	v_fmac_f32_e32 v34, v56, v56
	v_add_f32_e32 v33, v33, v34
	v_add_f32_e32 v32, v32, v33
	s_nop 1
	v_mov_b32_dpp v33, v32 quad_perm:[1,0,3,2] row_mask:0xf bank_mask:0xf
	s_mov_b64 s[14:15], 0xed40800
	v_lshl_add_u64 v[92:93], v[72:73], 0, s[14:15]
	v_cvt_pk_bf16_f32 v34, v54, v55
	s_mov_b64 s[14:15], 0xed40c00
	s_waitcnt lgkmcnt(0)
	v_add_f32_e32 v32, v32, v33
	s_nop 1
	v_mov_b32_dpp v33, v32 quad_perm:[2,3,0,1] row_mask:0xf bank_mask:0xf
	v_lshl_add_u64 v[72:73], v[72:73], 0, s[14:15]
	v_lshl_add_u64 v[66:67], v[66:67], 0, s[80:81]
	v_lshl_add_u64 v[68:69], v[68:69], 0, s[84:85]
	s_mov_b32 s14, s7
	s_waitcnt lgkmcnt(0)
	v_add_f32_e32 v32, v32, v33
	s_nop 1
	v_mov_b32_dpp v33, v32 row_half_mirror row_mask:0xf bank_mask:0xf
	s_waitcnt lgkmcnt(0)
	v_add_f32_e32 v35, v32, v33
	s_nop 1
	v_mov_b32_dpp v96, v35 row_mirror row_mask:0xf bank_mask:0xf
	v_cvt_pk_bf16_f32 v32, v52, v53
	v_cvt_pk_bf16_f32 v33, v36, v37
	s_waitcnt lgkmcnt(0)
	v_add_f32_e32 v96, v35, v96
	ds_swizzle_b32 v97, v96 offset:swizzle(SWAP,16)
	v_cvt_pk_bf16_f32 v35, v38, v39
	global_store_dwordx4 v[92:93], v[32:35], off
	s_waitcnt lgkmcnt(0)
	s_nop 0
	v_add_f32_e32 v34, v96, v97
	v_mov_b32_e32 v35, v34
	s_nop 1
	v_permlane32_swap_b32_e32 v34, v35
	v_add_f32_e32 v34, v34, v35
	v_fmamk_f32 v34, v34, 0x3a800000, v196
	v_mul_f32_e32 v35, 0x4b800000, v34
	v_cmp_gt_f32_e32 vcc, s35, v34
	v_cvt_pk_bf16_f32 v32, v86, v87
	v_cvt_pk_bf16_f32 v33, v94, v95
	v_cndmask_b32_e32 v34, v34, v35, vcc
	v_rsq_f32_e32 v92, v34
	v_cvt_pk_bf16_f32 v34, v58, v59
	v_cvt_pk_bf16_f32 v35, v56, v57
	global_store_dwordx4 v[72:73], v[32:35], off
	s_nop 1
	v_mul_f32_e32 v32, 0x45800000, v92
	v_cndmask_b32_e32 v72, v92, v32, vcc
	v_pk_mul_f32 v[32:33], v[52:53], v[72:73] op_sel_hi:[1,0]
	v_pk_mul_f32 v[34:35], v[36:37], v[72:73] op_sel_hi:[1,0]
	v_pk_mul_f32 v[36:37], v[54:55], v[72:73] op_sel_hi:[1,0]
	v_pk_fma_f32 v[32:33], v[74:75], v[32:33], v[28:29]
	v_pk_fma_f32 v[36:37], v[80:81], v[36:37], v[24:25]
	v_mov_b32_e32 v52, v113
	v_mov_b32_e32 v53, v113
	v_cvt_pk_fp8_f32 v52, v32, v33
	v_cvt_pk_fp8_f32 v53, v36, v37
	v_pk_mul_f32 v[38:39], v[38:39], v[72:73] op_sel_hi:[1,0]
	v_pk_fma_f32 v[34:35], v[76:77], v[34:35], v[30:31]
	v_pk_fma_f32 v[38:39], v[78:79], v[38:39], v[26:27]
	v_cvt_pk_fp8_f32 v52, v34, v35 op_sel:[0,0,1]
	v_cvt_pk_fp8_f32 v53, v38, v39 op_sel:[0,0,1]
	v_cvt_pk_bf16_f32 v32, v32, v33
	v_cvt_pk_bf16_f32 v33, v34, v35
	v_cvt_pk_bf16_f32 v34, v36, v37
	v_cvt_pk_bf16_f32 v35, v38, v39
	global_store_dwordx4 v[48:49], v[32:35], off offset:2048
	global_store_dwordx2 v[50:51], v[52:53], off offset:1024
	v_pk_mul_f32 v[36:37], v[58:59], v[72:73] op_sel_hi:[1,0]
	v_pk_mul_f32 v[32:33], v[86:87], v[72:73] op_sel_hi:[1,0]
	s_waitcnt vmcnt(5)
	v_pk_fma_f32 v[36:37], v[90:91], v[36:37], v[40:41]
	s_waitcnt vmcnt(4)
	v_pk_fma_f32 v[32:33], v[84:85], v[32:33], v[44:45]
	v_mov_b32_e32 v52, v113
	v_mov_b32_e32 v53, v113
	v_cvt_pk_fp8_f32 v52, v32, v33
	v_cvt_pk_fp8_f32 v53, v36, v37
	v_pk_mul_f32 v[34:35], v[94:95], v[72:73] op_sel_hi:[1,0]
	v_pk_mul_f32 v[38:39], v[56:57], v[72:73] op_sel_hi:[1,0]
	v_pk_fma_f32 v[34:35], v[82:83], v[34:35], v[46:47]
	v_pk_fma_f32 v[38:39], v[88:89], v[38:39], v[42:43]
	v_cvt_pk_fp8_f32 v52, v34, v35 op_sel:[0,0,1]
	v_cvt_pk_fp8_f32 v53, v38, v39 op_sel:[0,0,1]
	v_cvt_pk_bf16_f32 v32, v32, v33
	v_cvt_pk_bf16_f32 v33, v34, v35
	v_cvt_pk_bf16_f32 v34, v36, v37
	v_cvt_pk_bf16_f32 v35, v38, v39
	global_store_dwordx4 v[48:49], v[32:35], off offset:3072
	global_store_dwordx2 v[50:51], v[52:53], off offset:1536
	v_mov_b64_e32 v[58:59], v[10:11]
	v_mov_b64_e32 v[34:35], v[14:15]
	s_andn2_b64 vcc, exec, s[38:39]
	v_mov_b64_e32 v[32:33], v[12:13]
	v_mov_b64_e32 v[56:57], v[8:9]
	s_cbranch_vccz .LBB0_145

.LBB0_143:
	s_waitcnt vmcnt(17)
	v_cvt_pk_f32_fp8_sdwa v[120:121], v118 src0_sel:WORD_1
	v_cvt_pk_f32_fp8_e32 v[122:123], v118
	v_cvt_pk_f32_fp8_sdwa v[124:125], v119 src0_sel:WORD_1
	s_waitcnt vmcnt(16)
	v_cvt_pk_f32_fp8_e32 v[126:127], v116
	v_cvt_pk_f32_fp8_sdwa v[128:129], v116 src0_sel:WORD_1
	v_cvt_pk_f32_fp8_e32 v[130:131], v117
	v_cvt_pk_f32_fp8_sdwa v[116:117], v117 src0_sel:WORD_1
	v_cvt_pk_f32_fp8_e32 v[118:119], v119
	v_pk_add_f32 v[120:121], v[120:121], 0 op_sel_hi:[1,0]
	v_pk_add_f32 v[122:123], v[122:123], 0 op_sel_hi:[1,0]
	v_pk_add_f32 v[124:125], v[124:125], 0 op_sel_hi:[1,0]
	v_pk_add_f32 v[122:123], v[122:123], v[126:127]
	v_pk_add_f32 v[120:121], v[120:121], v[128:129]
	v_pk_add_f32 v[116:117], v[124:125], v[116:117]
	s_waitcnt vmcnt(13)
	v_cvt_pk_f32_fp8_sdwa v[124:125], v114 src0_sel:WORD_1
	v_cvt_pk_f32_fp8_e32 v[126:127], v114
	v_cvt_pk_f32_fp8_sdwa v[128:129], v115 src0_sel:WORD_1
	v_cvt_pk_f32_fp8_e32 v[114:115], v115
	v_pk_add_f32 v[118:119], v[118:119], 0 op_sel_hi:[1,0]
	v_pk_add_f32 v[120:121], v[120:121], v[124:125]
	v_pk_add_f32 v[118:119], v[118:119], v[130:131]
	v_pk_add_f32 v[122:123], v[122:123], v[126:127]
	v_pk_add_f32 v[114:115], v[118:119], v[114:115]
	s_waitcnt vmcnt(12)
	v_cvt_pk_f32_fp8_e32 v[118:119], v110
	v_cvt_pk_f32_fp8_sdwa v[124:125], v110 src0_sel:WORD_1
	v_cvt_pk_f32_fp8_e32 v[126:127], v111
	v_cvt_pk_f32_fp8_sdwa v[110:111], v111 src0_sel:WORD_1
	v_pk_add_f32 v[116:117], v[116:117], v[128:129]
	v_pk_add_f32 v[118:119], v[122:123], v[118:119]
	v_pk_add_f32 v[120:121], v[120:121], v[124:125]
	v_pk_add_f32 v[114:115], v[114:115], v[126:127]
	v_pk_add_f32 v[110:111], v[116:117], v[110:111]
	v_lshlrev_b32_e32 v116, 16, v52
	v_and_b32_e32 v117, 0xffff0000, v52
	v_lshlrev_b32_e32 v52, 16, v53
	v_and_b32_e32 v53, 0xffff0000, v53
	v_lshlrev_b32_e32 v122, 16, v54
	v_and_b32_e32 v123, 0xffff0000, v54
	v_lshlrev_b32_e32 v54, 16, v55
	v_and_b32_e32 v55, 0xffff0000, v55
	v_pk_fma_f32 v[52:53], v[2:3], v[120:121], v[52:53]
	v_pk_fma_f32 v[116:117], v[0:1], v[118:119], v[116:117]
	v_pk_fma_f32 v[54:55], v[6:7], v[110:111], v[54:55]
	v_pk_fma_f32 v[110:111], v[4:5], v[114:115], v[122:123]
	v_cvt_pk_f32_fp8_sdwa v[114:115], v108 src0_sel:WORD_1
	v_cvt_pk_f32_fp8_e32 v[118:119], v108
	v_cvt_pk_f32_fp8_sdwa v[120:121], v109 src0_sel:WORD_1
	v_cvt_pk_f32_fp8_e32 v[122:123], v106
	v_cvt_pk_f32_fp8_sdwa v[124:125], v106 src0_sel:WORD_1
	v_cvt_pk_f32_fp8_e32 v[126:127], v107
	v_cvt_pk_f32_fp8_sdwa v[106:107], v107 src0_sel:WORD_1
	v_cvt_pk_f32_fp8_e32 v[108:109], v109
	v_pk_add_f32 v[114:115], v[114:115], 0 op_sel_hi:[1,0]
	v_pk_add_f32 v[118:119], v[118:119], 0 op_sel_hi:[1,0]
	v_pk_add_f32 v[120:121], v[120:121], 0 op_sel_hi:[1,0]
	v_pk_add_f32 v[118:119], v[118:119], v[122:123]
	v_pk_add_f32 v[114:115], v[114:115], v[124:125]
	v_pk_add_f32 v[106:107], v[120:121], v[106:107]
	s_waitcnt vmcnt(10)
	v_cvt_pk_f32_fp8_sdwa v[120:121], v104 src0_sel:WORD_1
	v_cvt_pk_f32_fp8_e32 v[122:123], v104
	v_cvt_pk_f32_fp8_sdwa v[124:125], v105 src0_sel:WORD_1
	v_cvt_pk_f32_fp8_e32 v[104:105], v105
	v_pk_add_f32 v[108:109], v[108:109], 0 op_sel_hi:[1,0]
	v_pk_add_f32 v[114:115], v[114:115], v[120:121]
	v_pk_add_f32 v[108:109], v[108:109], v[126:127]
	v_pk_add_f32 v[118:119], v[118:119], v[122:123]
	v_pk_add_f32 v[104:105], v[108:109], v[104:105]
	v_cvt_pk_f32_fp8_e32 v[108:109], v102
	v_cvt_pk_f32_fp8_sdwa v[120:121], v102 src0_sel:WORD_1
	v_cvt_pk_f32_fp8_e32 v[122:123], v103
	v_cvt_pk_f32_fp8_sdwa v[102:103], v103 src0_sel:WORD_1
	v_pk_add_f32 v[106:107], v[106:107], v[124:125]
	v_pk_add_f32 v[114:115], v[114:115], v[120:121]
	v_pk_add_f32 v[108:109], v[118:119], v[108:109]
	v_pk_add_f32 v[102:103], v[106:107], v[102:103]
	v_lshlrev_b32_e32 v106, 16, v48
	v_and_b32_e32 v107, 0xffff0000, v48
	v_lshlrev_b32_e32 v48, 16, v49
	v_and_b32_e32 v49, 0xffff0000, v49
	v_pk_fma_f32 v[114:115], v[18:19], v[114:115], v[48:49]
	v_mul_f32_e32 v48, v117, v117
	v_mul_f32_e32 v49, v53, v53
	v_lshlrev_b32_e32 v118, 16, v50
	v_and_b32_e32 v119, 0xffff0000, v50
	v_lshlrev_b32_e32 v50, 16, v51
	v_and_b32_e32 v51, 0xffff0000, v51
	v_fmac_f32_e32 v48, v116, v116
	v_fmac_f32_e32 v49, v52, v52
	v_pk_fma_f32 v[102:103], v[22:23], v[102:103], v[50:51]
	v_add_f32_e32 v48, v48, v49
	v_mul_f32_e32 v49, v111, v111
	v_mul_f32_e32 v50, v55, v55
	v_fmac_f32_e32 v49, v110, v110
	v_fmac_f32_e32 v50, v54, v54
	v_pk_fma_f32 v[106:107], v[16:17], v[108:109], v[106:107]
	v_add_f32_e32 v49, v49, v50
	v_add_f32_e32 v48, v48, v49
	v_mul_f32_e32 v49, v107, v107
	v_mul_f32_e32 v50, v115, v115
	v_pk_add_f32 v[104:105], v[104:105], v[122:123]
	v_fmac_f32_e32 v49, v106, v106
	v_fmac_f32_e32 v50, v114, v114
	v_pk_fma_f32 v[104:105], v[20:21], v[104:105], v[118:119]
	v_add_f32_e32 v49, v49, v50
	v_add_f32_e32 v48, v48, v49
	v_mul_f32_e32 v49, v105, v105
	v_mul_f32_e32 v50, v103, v103
	v_fmac_f32_e32 v49, v104, v104
	v_fmac_f32_e32 v50, v102, v102
	v_add_f32_e32 v49, v49, v50
	v_add_f32_e32 v48, v48, v49
	s_nop 1
	v_mov_b32_dpp v49, v48 quad_perm:[1,0,3,2] row_mask:0xf bank_mask:0xf
	s_mov_b64 s[26:27], 0xed40000
	v_lshl_add_u64 v[108:109], v[72:73], 0, s[26:27]
	v_cvt_pk_bf16_f32 v50, v110, v111
	s_mov_b64 s[26:27], 0xed40400
	s_waitcnt lgkmcnt(0)
	v_add_f32_e32 v48, v48, v49
	s_nop 1
	v_mov_b32_dpp v49, v48 quad_perm:[2,3,0,1] row_mask:0xf bank_mask:0xf
	s_mov_b32 s15, s13
	v_lshl_add_u64 v[118:119], v[72:73], 0, s[26:27]
	s_add_i32 s13, s14, 1
	s_mul_hi_i32 s14, s13, 0x78787879
	s_waitcnt lgkmcnt(0)
	v_add_f32_e32 v48, v48, v49
	s_nop 1
	v_mov_b32_dpp v49, v48 row_half_mirror row_mask:0xf bank_mask:0xf
	s_lshr_b32 s25, s14, 31
	s_ashr_i32 s14, s14, 11
	s_add_i32 s14, s14, s25
	s_mul_i32 s25, s14, 0xffffef00
	s_waitcnt lgkmcnt(0)
	v_add_f32_e32 v51, v48, v49
	s_nop 1
	v_mov_b32_dpp v112, v51 row_mirror row_mask:0xf bank_mask:0xf
	v_cvt_pk_bf16_f32 v48, v116, v117
	v_cvt_pk_bf16_f32 v49, v52, v53
	s_add_i32 s13, s13, s25
	s_cmpk_gt_i32 s13, 0xff
	s_waitcnt lgkmcnt(0)
	v_add_f32_e32 v112, v51, v112
	ds_swizzle_b32 v120, v112 offset:swizzle(SWAP,16)
	v_cvt_pk_bf16_f32 v51, v54, v55
	global_store_dwordx4 v[108:109], v[48:51], off
	s_cselect_b32 s13, s14, 16
	s_mov_b32 s14, 0x17dd9000
	s_waitcnt lgkmcnt(0)
	v_add_f32_e32 v50, v112, v120
	v_mov_b32_e32 v51, v50
	s_nop 1
	v_permlane32_swap_b32_e32 v50, v51
	v_add_f32_e32 v50, v50, v51
	v_fmamk_f32 v50, v50, 0x3a800000, v196
	v_mul_f32_e32 v51, 0x4b800000, v50
	v_cmp_gt_f32_e32 vcc, s35, v50
	v_cvt_pk_bf16_f32 v48, v106, v107
	v_cvt_pk_bf16_f32 v49, v114, v115
	v_cndmask_b32_e32 v50, v50, v51, vcc
	v_rsq_f32_e32 v108, v50
	v_cvt_pk_bf16_f32 v50, v104, v105
	v_cvt_pk_bf16_f32 v51, v102, v103
	global_store_dwordx4 v[118:119], v[48:51], off
	v_mov_b32_e32 v119, v113
	v_mov_b32_e32 v118, v113
	v_mul_f32_e32 v48, 0x45800000, v108
	v_cndmask_b32_e32 v108, v108, v48, vcc
	v_pk_mul_f32 v[50:51], v[52:53], v[108:109] op_sel_hi:[1,0]
	v_pk_mul_f32 v[48:49], v[116:117], v[108:109] op_sel_hi:[1,0]
	v_pk_fma_f32 v[116:117], v[76:77], v[50:51], v[30:31]
	v_pk_mul_f32 v[50:51], v[110:111], v[108:109] op_sel_hi:[1,0]
	v_pk_fma_f32 v[48:49], v[74:75], v[48:49], v[28:29]
	v_pk_fma_f32 v[110:111], v[80:81], v[50:51], v[24:25]
	v_pk_mul_f32 v[52:53], v[54:55], v[108:109] op_sel_hi:[1,0]
	v_cvt_pk_fp8_f32 v119, v110, v111
	v_pk_fma_f32 v[54:55], v[78:79], v[52:53], v[26:27]
	v_cvt_pk_bf16_f32 v50, v48, v49
	v_cvt_pk_fp8_f32 v118, v48, v49
	v_add_co_u32_e32 v48, vcc, s14, v72
	v_cvt_pk_bf16_f32 v51, v116, v117
	v_cvt_pk_bf16_f32 v52, v110, v111
	v_cvt_pk_bf16_f32 v53, v54, v55
	v_addc_co_u32_e32 v49, vcc, 0, v73, vcc
	global_store_dwordx4 v[48:49], v[50:53], off
	v_cvt_pk_fp8_f32 v119, v54, v55 op_sel:[0,0,1]
	v_pk_mul_f32 v[54:55], v[114:115], v[108:109] op_sel_hi:[1,0]
	v_pk_mul_f32 v[52:53], v[106:107], v[108:109] op_sel_hi:[1,0]
	s_waitcnt vmcnt(3)
	v_pk_fma_f32 v[106:107], v[82:83], v[54:55], v[46:47]
	v_pk_fma_f32 v[54:55], v[84:85], v[52:53], v[44:45]
	v_pk_mul_f32 v[52:53], v[104:105], v[108:109] op_sel_hi:[1,0]
	v_pk_mul_f32 v[102:103], v[102:103], v[108:109] op_sel_hi:[1,0]
	v_pk_fma_f32 v[104:105], v[90:91], v[52:53], v[40:41]
	v_mov_b32_e32 v108, v113
	v_mov_b32_e32 v109, v113
	v_cvt_pk_fp8_f32 v108, v54, v55
	v_cvt_pk_fp8_f32 v109, v104, v105
	v_pk_fma_f32 v[102:103], v[88:89], v[102:103], v[42:43]
	v_cvt_pk_fp8_f32 v118, v116, v117 op_sel:[0,0,1]
	v_cvt_pk_fp8_f32 v108, v106, v107 op_sel:[0,0,1]
	v_cvt_pk_fp8_f32 v109, v102, v103 op_sel:[0,0,1]
	v_lshl_add_u64 v[50:51], s[94:95], 0, v[66:67]
	s_mov_b32 s14, 0x711d9000
	v_add_co_u32_e32 v50, vcc, s14, v50
	v_cvt_pk_bf16_f32 v52, v54, v55
	s_nop 0
	v_addc_co_u32_e32 v51, vcc, 0, v51, vcc
	v_cvt_pk_bf16_f32 v53, v106, v107
	v_cvt_pk_bf16_f32 v54, v104, v105
	v_cvt_pk_bf16_f32 v55, v102, v103
	s_cmp_eq_u32 s13, s15
	global_store_dwordx2 v[50:51], v[118:119], off
	global_store_dwordx4 v[48:49], v[52:55], off offset:1024
	global_store_dwordx2 v[50:51], v[108:109], off offset:512
	s_cbranch_scc1 .LBB0_140
	s_mul_i32 s25, s13, 0x6000
	s_mul_hi_i32 s15, s13, 0x6000
	s_add_u32 s14, s60, s25
	s_addc_u32 s15, s63, s15
	v_lshl_add_u64 v[0:1], s[14:15], 0, v[70:71]
	s_mov_b64 s[14:15], 0x5000
	v_lshl_add_u64 v[16:17], v[0:1], 0, s[14:15]
	v_add_co_u32_e32 v0, vcc, 0x5000, v0
	s_mov_b32 s14, 0x3d800000
	s_nop 0
	v_addc_co_u32_e32 v1, vcc, 0, v1, vcc
	global_load_dwordx4 v[0:3], v[0:1], off
	s_nop 0
	global_load_dwordx4 v[4:7], v[16:17], off offset:16
	global_load_dwordx4 v[20:23], v[16:17], off offset:2064
	s_nop 0
	global_load_dwordx4 v[16:19], v[16:17], off offset:2048
	s_add_i32 s25, s25, 0x66000
	global_load_dwordx4 v[24:27], v[64:65], off offset:16
	global_load_dwordx4 v[28:31], v[64:65], off
	s_waitcnt vmcnt(5)
	v_pk_mul_f32 v[2:3], v[2:3], s[14:15] op_sel_hi:[1,0]
	v_pk_mul_f32 v[0:1], v[0:1], s[14:15] op_sel_hi:[1,0]
	s_waitcnt vmcnt(4)
	v_pk_mul_f32 v[6:7], v[6:7], s[14:15] op_sel_hi:[1,0]
	v_pk_mul_f32 v[4:5], v[4:5], s[14:15] op_sel_hi:[1,0]
	s_waitcnt vmcnt(2)
	v_pk_mul_f32 v[18:19], v[18:19], s[14:15] op_sel_hi:[1,0]
	v_pk_mul_f32 v[16:17], v[16:17], s[14:15] op_sel_hi:[1,0]
	v_pk_mul_f32 v[22:23], v[22:23], s[14:15] op_sel_hi:[1,0]
	v_pk_mul_f32 v[20:21], v[20:21], s[14:15] op_sel_hi:[1,0]
	s_add_i32 s14, s13, 17
	s_mul_hi_i32 s15, s14, 0x6000
	s_add_u32 s14, s60, s25
	s_addc_u32 s15, s63, s15
	v_lshl_add_u64 v[102:103], s[14:15], 0, v[70:71]
	s_movk_i32 s14, 0x1000
	v_add_co_u32_e32 v40, vcc, s14, v102
	v_lshl_add_u64 v[82:83], v[102:103], 0, s[84:85]
	s_nop 0
	v_addc_co_u32_e32 v41, vcc, 0, v103, vcc
	global_load_dwordx4 v[40:43], v[40:41], off
	s_nop 0
	global_load_dwordx4 v[44:47], v[82:83], off offset:16
	s_waitcnt vmcnt(1)
	v_pk_add_f32 v[42:43], v[42:43], 1.0 op_sel_hi:[1,0]
	v_pk_add_f32 v[40:41], v[40:41], 1.0 op_sel_hi:[1,0]
	v_pk_mul_f32 v[76:77], v[30:31], v[42:43]
	v_pk_mul_f32 v[74:75], v[28:29], v[40:41]
	s_waitcnt vmcnt(0)
	v_pk_add_f32 v[28:29], v[46:47], 1.0 op_sel_hi:[1,0]
	v_pk_add_f32 v[30:31], v[44:45], 1.0 op_sel_hi:[1,0]
	v_pk_mul_f32 v[78:79], v[26:27], v[28:29]
	v_pk_mul_f32 v[80:81], v[24:25], v[30:31]
	global_load_dwordx4 v[24:27], v[102:103], off offset:16
	global_load_dwordx4 v[28:31], v[102:103], off
	global_load_dwordx4 v[40:43], v[64:65], off offset:2064
	global_load_dwordx4 v[44:47], v[64:65], off offset:2048
	global_load_dwordx4 v[52:55], v[82:83], off offset:2064
	s_nop 0
	global_load_dwordx4 v[82:85], v[82:83], off offset:2048
	s_waitcnt vmcnt(0)
	v_pk_add_f32 v[84:85], v[84:85], 1.0 op_sel_hi:[1,0]
	v_pk_add_f32 v[88:89], v[82:83], 1.0 op_sel_hi:[1,0]
	v_pk_mul_f32 v[82:83], v[46:47], v[84:85]
	v_pk_mul_f32 v[84:85], v[44:45], v[88:89]
	v_pk_add_f32 v[44:45], v[54:55], 1.0 op_sel_hi:[1,0]
	v_pk_add_f32 v[46:47], v[52:53], 1.0 op_sel_hi:[1,0]
	v_pk_mul_f32 v[88:89], v[42:43], v[44:45]
	v_pk_mul_f32 v[90:91], v[40:41], v[46:47]
	global_load_dwordx4 v[40:43], v[102:103], off offset:2064
	global_load_dwordx4 v[44:47], v[102:103], off offset:2048
	s_branch .LBB0_140

.LBB0_148:
	v_mul_f32_e32 v32, v21, v21
	v_mul_f32_e32 v33, v23, v23
	v_fmac_f32_e32 v32, v20, v20
	v_fmac_f32_e32 v33, v22, v22
	v_add_f32_e32 v32, v32, v33
	v_mul_f32_e32 v33, v17, v17
	v_mul_f32_e32 v34, v19, v19
	v_fmac_f32_e32 v33, v16, v16
	v_fmac_f32_e32 v34, v18, v18
	v_add_f32_e32 v33, v33, v34
	v_add_f32_e32 v32, v32, v33
	v_mul_f32_e32 v33, v13, v13
	v_mul_f32_e32 v34, v15, v15
	v_fmac_f32_e32 v33, v12, v12
	v_fmac_f32_e32 v34, v14, v14
	v_add_f32_e32 v33, v33, v34
	v_add_f32_e32 v32, v32, v33
	v_mul_f32_e32 v33, v9, v9
	v_mul_f32_e32 v34, v11, v11
	v_fmac_f32_e32 v33, v8, v8
	v_fmac_f32_e32 v34, v10, v10
	v_add_f32_e32 v33, v33, v34
	v_add_f32_e32 v32, v32, v33
	s_nop 1
	v_mov_b32_dpp v33, v32 quad_perm:[1,0,3,2] row_mask:0xf bank_mask:0xf
	v_lshl_add_u64 v[50:51], v[50:51], 0, s[80:81]
	v_lshl_add_u64 v[52:53], v[52:53], 0, s[84:85]
	s_cmp_ge_i32 s2, s12
	s_waitcnt lgkmcnt(0)
	v_add_f32_e32 v32, v32, v33
	s_nop 1
	v_mov_b32_dpp v33, v32 quad_perm:[2,3,0,1] row_mask:0xf bank_mask:0xf
	s_waitcnt lgkmcnt(0)
	v_add_f32_e32 v32, v32, v33
	s_nop 1
	v_mov_b32_dpp v33, v32 row_half_mirror row_mask:0xf bank_mask:0xf
	s_waitcnt lgkmcnt(0)
	v_add_f32_e32 v32, v32, v33
	s_nop 1
	v_mov_b32_dpp v33, v32 row_mirror row_mask:0xf bank_mask:0xf
	s_waitcnt lgkmcnt(0)
	v_add_f32_e32 v32, v32, v33
	ds_swizzle_b32 v33, v32 offset:swizzle(SWAP,16)
	s_waitcnt lgkmcnt(0)
	v_add_f32_e32 v32, v32, v33
	v_mov_b32_e32 v33, v32
	s_nop 1
	v_permlane32_swap_b32_e32 v32, v33
	v_add_f32_e32 v32, v32, v33
	v_fmamk_f32 v32, v32, 0x3a800000, v196
	v_cmp_gt_f32_e32 vcc, s35, v32
	v_mul_f32_e32 v33, 0x4b800000, v32
	s_nop 0
	v_cndmask_b32_e32 v32, v32, v33, vcc
	v_rsq_f32_e32 v32, v32
	s_nop 0
	v_mul_f32_e32 v33, 0x45800000, v32
	v_cndmask_b32_e32 v32, v32, v33, vcc
	v_pk_mul_f32 v[20:21], v[20:21], v[32:33] op_sel_hi:[1,0]
	v_pk_mul_f32 v[22:23], v[22:23], v[32:33] op_sel_hi:[1,0]
	v_pk_mul_f32 v[16:17], v[16:17], v[32:33] op_sel_hi:[1,0]
	v_pk_mul_f32 v[18:19], v[18:19], v[32:33] op_sel_hi:[1,0]
	v_pk_fma_f32 v[22:23], v[56:57], v[22:23], v[2:3]
	v_pk_fma_f32 v[20:21], v[54:55], v[20:21], v[0:1]
	v_pk_fma_f32 v[34:35], v[58:59], v[18:19], v[6:7]
	v_pk_fma_f32 v[36:37], v[62:63], v[16:17], v[4:5]
	v_cvt_pk_bf16_f32 v16, v20, v21
	v_cvt_pk_bf16_f32 v17, v22, v23
	v_cvt_pk_bf16_f32 v18, v36, v37
	v_cvt_pk_bf16_f32 v19, v34, v35
	global_store_dwordx4 v[42:43], v[16:19], off offset:2048
	v_pk_mul_f32 v[12:13], v[12:13], v[32:33] op_sel_hi:[1,0]
	v_pk_mul_f32 v[14:15], v[14:15], v[32:33] op_sel_hi:[1,0]
	v_mov_b32_e32 v16, v113
	v_mov_b32_e32 v17, v113
	v_cvt_pk_fp8_f32 v16, v20, v21
	v_cvt_pk_fp8_f32 v17, v36, v37
	v_pk_mul_f32 v[8:9], v[8:9], v[32:33] op_sel_hi:[1,0]
	v_pk_mul_f32 v[10:11], v[10:11], v[32:33] op_sel_hi:[1,0]
	v_cvt_pk_fp8_f32 v16, v22, v23 op_sel:[0,0,1]
	v_cvt_pk_fp8_f32 v17, v34, v35 op_sel:[0,0,1]
	s_waitcnt vmcnt(1)
	v_pk_fma_f32 v[14:15], v[64:65], v[14:15], v[30:31]
	v_pk_fma_f32 v[12:13], v[66:67], v[12:13], v[28:29]
	v_pk_fma_f32 v[18:19], v[70:71], v[8:9], v[24:25]
	global_store_dwordx2 v[40:41], v[16:17], off offset:1024
	v_pk_fma_f32 v[16:17], v[68:69], v[10:11], v[26:27]
	v_cvt_pk_bf16_f32 v8, v12, v13
	v_cvt_pk_bf16_f32 v9, v14, v15
	v_cvt_pk_bf16_f32 v10, v18, v19
	v_cvt_pk_bf16_f32 v11, v16, v17
	global_store_dwordx4 v[42:43], v[8:11], off offset:3072
	s_nop 1
	v_mov_b32_e32 v8, v113
	v_mov_b32_e32 v9, v113
	v_cvt_pk_fp8_f32 v8, v12, v13
	v_cvt_pk_fp8_f32 v9, v18, v19
	v_cvt_pk_fp8_f32 v8, v14, v15 op_sel:[0,0,1]
	v_cvt_pk_fp8_f32 v9, v16, v17 op_sel:[0,0,1]
	global_store_dwordx2 v[40:41], v[8:9], off offset:1536
	s_cbranch_scc1 .LBB0_153

.LBB0_151:
	s_waitcnt vmcnt(0)
	v_mul_f32_e32 v72, v45, v45
	v_mul_f32_e32 v73, v47, v47
	v_fmac_f32_e32 v72, v44, v44
	v_fmac_f32_e32 v73, v46, v46
	v_add_f32_e32 v72, v72, v73
	v_mul_f32_e32 v73, v41, v41
	v_mul_f32_e32 v74, v43, v43
	v_fmac_f32_e32 v73, v40, v40
	v_fmac_f32_e32 v74, v42, v42
	v_add_f32_e32 v73, v73, v74
	v_add_f32_e32 v72, v72, v73
	s_waitcnt vmcnt(4)
	v_mul_f32_e32 v73, v37, v37
	v_mul_f32_e32 v74, v39, v39
	v_fmac_f32_e32 v73, v36, v36
	v_fmac_f32_e32 v74, v38, v38
	v_add_f32_e32 v73, v73, v74
	v_add_f32_e32 v72, v72, v73
	v_mul_f32_e32 v73, v33, v33
	v_mul_f32_e32 v74, v35, v35
	v_fmac_f32_e32 v73, v32, v32
	v_fmac_f32_e32 v74, v34, v34
	v_add_f32_e32 v73, v73, v74
	v_add_f32_e32 v72, v72, v73
	s_nop 1
	v_mov_b32_dpp v73, v72 quad_perm:[1,0,3,2] row_mask:0xf bank_mask:0xf
	s_and_b64 s[14:15], s[38:39], exec
	s_mov_b32 s7, s4
	s_cselect_b32 s4, 16, s6
	s_mov_b32 s6, 0x17dd9000
	s_waitcnt lgkmcnt(0)
	v_add_f32_e32 v72, v72, v73
	s_nop 1
	v_mov_b32_dpp v73, v72 quad_perm:[2,3,0,1] row_mask:0xf bank_mask:0xf
	s_cmp_eq_u32 s4, s7
	s_waitcnt lgkmcnt(0)
	v_add_f32_e32 v72, v72, v73
	s_nop 1
	v_mov_b32_dpp v73, v72 row_half_mirror row_mask:0xf bank_mask:0xf
	s_waitcnt lgkmcnt(0)
	v_add_f32_e32 v72, v72, v73
	s_nop 1
	v_mov_b32_dpp v73, v72 row_mirror row_mask:0xf bank_mask:0xf
	s_waitcnt lgkmcnt(0)
	v_add_f32_e32 v72, v72, v73
	ds_swizzle_b32 v73, v72 offset:swizzle(SWAP,16)
	s_waitcnt lgkmcnt(0)
	v_add_f32_e32 v72, v72, v73
	v_mov_b32_e32 v73, v72
	s_nop 1
	v_permlane32_swap_b32_e32 v72, v73
	v_add_f32_e32 v72, v72, v73
	v_fmamk_f32 v72, v72, 0x3a800000, v196
	v_cmp_gt_f32_e32 vcc, s35, v72
	v_mul_f32_e32 v73, 0x4b800000, v72
	s_nop 0
	v_cndmask_b32_e32 v72, v72, v73, vcc
	v_rsq_f32_e32 v72, v72
	s_nop 0
	v_mul_f32_e32 v73, 0x45800000, v72
	v_cndmask_b32_e32 v72, v72, v73, vcc
	v_pk_mul_f32 v[42:43], v[42:43], v[72:73] op_sel_hi:[1,0]
	v_pk_mul_f32 v[44:45], v[44:45], v[72:73] op_sel_hi:[1,0]
	v_pk_mul_f32 v[46:47], v[46:47], v[72:73] op_sel_hi:[1,0]
	v_pk_mul_f32 v[40:41], v[40:41], v[72:73] op_sel_hi:[1,0]
	v_pk_fma_f32 v[78:79], v[58:59], v[42:43], v[6:7]
	v_lshl_add_u64 v[42:43], s[94:95], 0, v[52:53]
	v_pk_fma_f32 v[74:75], v[56:57], v[46:47], v[2:3]
	v_pk_fma_f32 v[76:77], v[54:55], v[44:45], v[0:1]
	v_pk_fma_f32 v[40:41], v[62:63], v[40:41], v[4:5]
	v_add_co_u32_e32 v42, vcc, s6, v42
	v_cvt_pk_bf16_f32 v44, v76, v77
	v_cvt_pk_bf16_f32 v45, v74, v75
	v_cvt_pk_bf16_f32 v46, v40, v41
	v_cvt_pk_bf16_f32 v47, v78, v79
	v_addc_co_u32_e32 v43, vcc, 0, v43, vcc
	global_store_dwordx4 v[42:43], v[44:47], off
	s_mov_b32 s6, 0x711d9000
	v_pk_mul_f32 v[36:37], v[36:37], v[72:73] op_sel_hi:[1,0]
	v_mov_b32_e32 v44, v113
	v_mov_b32_e32 v45, v113
	v_cvt_pk_fp8_f32 v44, v76, v77
	v_cvt_pk_fp8_f32 v45, v40, v41
	v_lshl_add_u64 v[40:41], s[94:95], 0, v[50:51]
	v_add_co_u32_e32 v40, vcc, s6, v40
	v_cvt_pk_fp8_f32 v44, v74, v75 op_sel:[0,0,1]
	v_cvt_pk_fp8_f32 v45, v78, v79 op_sel:[0,0,1]
	v_addc_co_u32_e32 v41, vcc, 0, v41, vcc
	v_pk_mul_f32 v[38:39], v[38:39], v[72:73] op_sel_hi:[1,0]
	v_pk_mul_f32 v[32:33], v[32:33], v[72:73] op_sel_hi:[1,0]
	v_pk_mul_f32 v[34:35], v[34:35], v[72:73] op_sel_hi:[1,0]
	global_store_dwordx2 v[40:41], v[44:45], off
	s_waitcnt vmcnt(2)
	v_pk_fma_f32 v[38:39], v[64:65], v[38:39], v[30:31]
	v_pk_fma_f32 v[36:37], v[66:67], v[36:37], v[28:29]
	v_pk_fma_f32 v[44:45], v[68:69], v[34:35], v[26:27]
	v_pk_fma_f32 v[46:47], v[70:71], v[32:33], v[24:25]
	v_cvt_pk_bf16_f32 v32, v36, v37
	v_cvt_pk_bf16_f32 v33, v38, v39
	v_cvt_pk_bf16_f32 v34, v46, v47
	v_cvt_pk_bf16_f32 v35, v44, v45
	global_store_dwordx4 v[42:43], v[32:35], off offset:1024
	s_nop 1
	v_mov_b32_e32 v32, v113
	v_mov_b32_e32 v33, v113
	v_cvt_pk_fp8_f32 v32, v36, v37
	v_cvt_pk_fp8_f32 v33, v46, v47
	v_cvt_pk_fp8_f32 v32, v38, v39 op_sel:[0,0,1]
	v_cvt_pk_fp8_f32 v33, v44, v45 op_sel:[0,0,1]
	global_store_dwordx2 v[40:41], v[32:33], off offset:512
	s_cbranch_scc1 .LBB0_148
	s_mul_i32 s6, s4, 0x6000
	s_mul_hi_i32 s7, s4, 0x6000
	s_add_u32 s6, s60, s6
	s_addc_u32 s7, s63, s7
	v_lshl_add_u64 v[44:45], v[60:61], 2, s[6:7]
	v_add_co_u32_e32 v24, vcc, 0x1000, v44
	global_load_dwordx4 v[0:3], v[48:49], off offset:16
	global_load_dwordx4 v[4:7], v[48:49], off
	v_addc_co_u32_e32 v25, vcc, 0, v45, vcc
	v_lshl_add_u64 v[36:37], v[44:45], 0, s[84:85]
	global_load_dwordx4 v[24:27], v[24:25], off
	s_nop 0
	global_load_dwordx4 v[28:31], v[36:37], off offset:16
	s_waitcnt vmcnt(1)
	v_pk_add_f32 v[26:27], v[26:27], 1.0 op_sel_hi:[1,0]
	v_pk_add_f32 v[24:25], v[24:25], 1.0 op_sel_hi:[1,0]
	v_pk_mul_f32 v[56:57], v[6:7], v[26:27]
	v_pk_mul_f32 v[54:55], v[4:5], v[24:25]
	s_waitcnt vmcnt(0)
	v_pk_add_f32 v[4:5], v[30:31], 1.0 op_sel_hi:[1,0]
	v_pk_add_f32 v[6:7], v[28:29], 1.0 op_sel_hi:[1,0]
	v_pk_mul_f32 v[58:59], v[2:3], v[4:5]
	v_pk_mul_f32 v[62:63], v[0:1], v[6:7]
	global_load_dwordx4 v[4:7], v[44:45], off offset:16
	global_load_dwordx4 v[0:3], v[44:45], off
	global_load_dwordx4 v[24:27], v[48:49], off offset:2064
	global_load_dwordx4 v[28:31], v[48:49], off offset:2048
	global_load_dwordx4 v[32:35], v[36:37], off offset:2064
	s_nop 0
	global_load_dwordx4 v[36:39], v[36:37], off offset:2048
	s_waitcnt vmcnt(0)
	v_pk_add_f32 v[38:39], v[38:39], 1.0 op_sel_hi:[1,0]
	v_pk_add_f32 v[36:37], v[36:37], 1.0 op_sel_hi:[1,0]
	v_pk_mul_f32 v[64:65], v[30:31], v[38:39]
	v_pk_mul_f32 v[66:67], v[28:29], v[36:37]
	v_pk_add_f32 v[28:29], v[34:35], 1.0 op_sel_hi:[1,0]
	v_pk_add_f32 v[30:31], v[32:33], 1.0 op_sel_hi:[1,0]
	v_pk_mul_f32 v[68:69], v[26:27], v[28:29]
	v_pk_mul_f32 v[70:71], v[24:25], v[30:31]
	global_load_dwordx4 v[24:27], v[44:45], off offset:2064
	global_load_dwordx4 v[28:31], v[44:45], off offset:2048
	s_branch .LBB0_148

.LBB0_343:
	s_add_i32 s70, s6, -3
	s_mul_hi_i32 s2, s70, 0x78787879
	s_lshr_b32 s7, s2, 31
	s_ashr_i32 s2, s2, 11
	s_add_i32 s2, s2, s7
	s_mulk_i32 s2, 0x1100
	s_sub_i32 s7, s70, s2
	s_cmpk_lt_i32 s7, 0x100
	s_movk_i32 s2, 0x1100
	s_cselect_b32 s2, 0x100, s2
	s_cselect_b32 s12, 0, 0x100
	s_add_i32 s13, s7, -2
	s_add_i32 s15, s2, -1
	s_add_i32 s14, s7, -1
	s_min_i32 s13, s13, s15
	s_min_i32 s14, s14, s15
	s_cmp_gt_i32 s7, s12
	s_cselect_b64 s[38:39], -1, 0
	s_and_b64 s[26:27], s[38:39], exec
	s_cselect_b32 s13, s13, s12
	s_cselect_b32 s14, s14, s12
	s_sub_i32 s13, s13, s7
	s_add_i32 s26, s70, s13
	s_ashr_i32 s27, s26, 31
	s_lshl_b64 s[26:27], s[26:27], 9
	v_lshl_add_u64 v[82:83], v[66:67], 0, s[26:27]
	global_load_dwordx2 v[94:95], v[82:83], off
	v_lshl_add_u64 v[82:83], v[68:69], 0, s[26:27]
	s_sub_i32 s13, s14, s7
	global_load_dwordx2 v[104:105], v[82:83], off
	v_lshl_add_u64 v[82:83], v[70:71], 0, s[26:27]
	s_add_i32 s26, s70, s13
	s_ashr_i32 s27, s26, 31
	s_lshl_b64 s[26:27], s[26:27], 9
	s_min_i32 s13, s7, s15
	global_load_dwordx2 v[106:107], v[82:83], off
	v_lshl_add_u64 v[82:83], v[66:67], 0, s[26:27]
	s_cmp_lt_i32 s7, s12
	global_load_dwordx2 v[108:109], v[82:83], off
	v_lshl_add_u64 v[82:83], v[68:69], 0, s[26:27]
	s_cselect_b64 s[40:41], -1, 0
	global_load_dwordx2 v[110:111], v[82:83], off
	v_lshl_add_u64 v[82:83], v[70:71], 0, s[26:27]
	s_and_b64 s[26:27], s[40:41], exec
	s_cselect_b32 s13, s12, s13
	s_sub_i32 s13, s13, s7
	s_add_i32 s26, s70, s13
	s_ashr_i32 s27, s26, 31
	s_or_b32 s14, s7, 1
	s_lshl_b64 s[26:27], s[26:27], 9
	s_min_i32 s13, s14, s15
	s_cmp_lt_i32 s14, s12
	global_load_dwordx2 v[114:115], v[82:83], off
	v_lshl_add_u64 v[82:83], v[66:67], 0, s[26:27]
	s_cselect_b32 s13, s12, s13
	global_load_dwordx2 v[116:117], v[82:83], off
	v_lshl_add_u64 v[82:83], v[68:69], 0, s[26:27]
	s_sub_i32 s13, s13, s7
	global_load_dwordx2 v[118:119], v[82:83], off
	v_lshl_add_u64 v[82:83], v[70:71], 0, s[26:27]
	s_add_i32 s26, s70, s13
	s_ashr_i32 s27, s26, 31
	s_or_b32 s25, s7, 2
	s_lshl_b64 s[42:43], s[26:27], 9
	s_min_i32 s13, s25, s15
	global_load_dwordx2 v[120:121], v[82:83], off
	v_add_u32_e32 v82, s70, v138
	s_cmp_lt_i32 s25, s12
	v_ashrrev_i32_e32 v83, 31, v82
	s_cselect_b32 s13, s12, s13
	v_lshlrev_b64 v[86:87], 9, v[82:83]
	s_sub_i32 s13, s13, s7
	v_lshl_add_u64 v[84:85], v[66:67], 0, s[42:43]
	v_lshl_add_u64 v[86:87], v[74:75], 0, v[86:87]
	s_add_i32 s26, s70, s13
	global_load_ushort v112, v[86:87], off
	global_load_dwordx2 v[126:127], v[84:85], off
	v_lshl_add_u64 v[84:85], v[68:69], 0, s[42:43]
	s_ashr_i32 s27, s26, 31
	global_load_dwordx2 v[140:141], v[84:85], off
	v_lshl_add_u64 v[84:85], v[70:71], 0, s[42:43]
	s_lshl_b64 s[26:27], s[26:27], 9
	global_load_dwordx2 v[142:143], v[84:85], off
	v_lshl_add_u64 v[84:85], v[66:67], 0, s[26:27]
	global_load_dwordx2 v[144:145], v[84:85], off
	v_lshl_add_u64 v[84:85], v[68:69], 0, s[26:27]
	global_load_dwordx2 v[146:147], v[84:85], off
	v_lshl_add_u64 v[84:85], v[70:71], 0, s[26:27]
	s_or_b32 s26, s7, 3
	s_min_i32 s13, s26, s15
	s_cmp_lt_i32 s26, s12
	s_cselect_b32 s13, s12, s13
	s_sub_i32 s13, s13, s7
	s_add_i32 s28, s70, s13
	s_ashr_i32 s29, s28, 31
	s_add_i32 s27, s7, 4
	s_lshl_b64 s[28:29], s[28:29], 9
	s_min_i32 s13, s27, s15
	s_cmp_lt_i32 s27, s12
	global_load_dwordx2 v[148:149], v[84:85], off
	v_lshl_add_u64 v[84:85], v[66:67], 0, s[28:29]
	s_cselect_b32 s13, s12, s13
	global_load_dwordx2 v[170:171], v[84:85], off
	v_lshl_add_u64 v[84:85], v[68:69], 0, s[28:29]
	s_sub_i32 s13, s13, s7
	global_load_dwordx2 v[172:173], v[84:85], off
	v_lshl_add_u64 v[84:85], v[70:71], 0, s[28:29]
	s_add_i32 s28, s70, s13
	s_ashr_i32 s29, s28, 31
	s_add_i32 s13, s7, 5
	s_lshl_b64 s[28:29], s[28:29], 9
	s_min_i32 s15, s13, s15
	s_cmp_lt_i32 s13, s12
	global_load_dwordx2 v[150:151], v[84:85], off
	v_lshl_add_u64 v[84:85], v[66:67], 0, s[28:29]
	s_cselect_b32 s15, s12, s15
	global_load_dwordx2 v[174:175], v[84:85], off
	v_lshl_add_u64 v[84:85], v[68:69], 0, s[28:29]
	s_sub_i32 s7, s15, s7
	global_load_dwordx2 v[176:177], v[84:85], off
	v_lshl_add_u64 v[84:85], v[70:71], 0, s[28:29]
	s_add_i32 s28, s70, s7
	s_ashr_i32 s29, s28, 31
	s_lshl_b64 s[28:29], s[28:29], 9
	global_load_dwordx2 v[178:179], v[84:85], off
	v_lshl_add_u64 v[84:85], v[66:67], 0, s[28:29]
	global_load_dwordx2 v[102:103], v[84:85], off
	v_lshl_add_u64 v[84:85], v[68:69], 0, s[28:29]
	s_ashr_i32 s71, s70, 31
	global_load_dwordx2 v[100:101], v[84:85], off
	v_lshl_add_u64 v[84:85], v[70:71], 0, s[28:29]
	s_lshl_b64 s[28:29], s[70:71], 9
	v_lshl_add_u64 v[96:97], v[72:73], 0, s[28:29]
	global_load_dwordx2 v[124:125], v[96:97], off
	global_load_dwordx2 v[98:99], v[84:85], off
	s_add_i32 s72, s6, -2
	s_ashr_i32 s73, s72, 31
	s_lshl_b64 s[28:29], s[72:73], 9
	v_lshl_add_u64 v[88:89], v[72:73], 0, s[28:29]
	global_load_dwordx2 v[122:123], v[88:89], off
	s_add_i32 s64, s6, -1
	s_ashr_i32 s65, s64, 31
	s_lshl_b64 s[28:29], s[64:65], 9
	s_ashr_i32 s7, s6, 31
	v_lshl_add_u64 v[86:87], v[72:73], 0, s[28:29]
	s_lshl_b64 s[28:29], s[6:7], 9
	s_cmp_ge_i32 s14, s12
	v_lshl_add_u64 v[84:85], v[72:73], 0, s[28:29]
	s_cselect_b64 s[28:29], -1, 0
	s_cmp_lt_i32 s14, s2
	s_cselect_b64 s[14:15], -1, 0
	s_waitcnt vmcnt(0)
	v_cndmask_b32_e64 v134, 0, v107, s[38:39]
	v_cndmask_b32_e64 v136, 0, v106, s[38:39]
	v_cndmask_b32_e64 v128, 0, v105, s[38:39]
	v_cndmask_b32_e64 v130, 0, v104, s[38:39]
	v_cndmask_b32_e64 v167, 0, v95, s[38:39]
	v_cndmask_b32_e64 v168, 0, v94, s[38:39]
	v_cndmask_b32_e64 v137, 0, v115, s[38:39]
	v_cndmask_b32_e64 v135, 0, v114, s[38:39]
	v_cndmask_b32_e64 v131, 0, v111, s[38:39]
	v_cndmask_b32_e64 v129, 0, v110, s[38:39]
	v_cndmask_b32_e64 v165, 0, v109, s[38:39]
	v_cndmask_b32_e64 v166, 0, v108, s[38:39]
	s_and_b64 s[38:39], s[28:29], s[14:15]
	s_cmp_ge_i32 s25, s12
	s_cselect_b64 s[14:15], -1, 0
	s_cmp_lt_i32 s25, s2
	s_cselect_b64 s[28:29], -1, 0
	v_cndmask_b32_e64 v157, v119, 0, s[40:41]
	v_cndmask_b32_e64 v161, v117, 0, s[40:41]
	v_cndmask_b32_e64 v132, 0, v143, s[38:39]
	v_cndmask_b32_e64 v156, 0, v142, s[38:39]
	v_cndmask_b32_e64 v119, 0, v141, s[38:39]
	v_cndmask_b32_e64 v159, 0, v140, s[38:39]
	v_cndmask_b32_e64 v117, 0, v127, s[38:39]
	v_cndmask_b32_e64 v163, 0, v126, s[38:39]
	s_and_b64 s[38:39], s[14:15], s[28:29]
	s_cmp_ge_i32 s26, s12
	s_cselect_b64 s[14:15], -1, 0
	s_cmp_lt_i32 s26, s2
	s_cselect_b64 s[28:29], -1, 0
	v_cndmask_b32_e64 v160, v118, 0, s[40:41]
	v_cndmask_b32_e64 v164, v116, 0, s[40:41]
	v_cndmask_b32_e64 v126, 0, v149, s[38:39]
	v_cndmask_b32_e64 v155, 0, v148, s[38:39]
	v_cndmask_b32_e64 v118, 0, v147, s[38:39]
	v_cndmask_b32_e64 v158, 0, v146, s[38:39]
	v_cndmask_b32_e64 v116, 0, v145, s[38:39]
	v_cndmask_b32_e64 v162, 0, v144, s[38:39]
	s_and_b64 s[38:39], s[14:15], s[28:29]
	s_cmp_ge_i32 s27, s12
	s_cselect_b64 s[14:15], -1, 0
	s_cmp_lt_i32 s27, s2
	s_cselect_b64 s[26:27], -1, 0
	v_cndmask_b32_e64 v151, 0, v151, s[38:39]
	v_cndmask_b32_e64 v152, 0, v150, s[38:39]
	v_cndmask_b32_e64 v153, 0, v173, s[38:39]
	v_cndmask_b32_e64 v154, 0, v172, s[38:39]
	v_cndmask_b32_e64 v133, 0, v171, s[38:39]
	v_cndmask_b32_e64 v127, 0, v170, s[38:39]
	s_and_b64 s[38:39], s[14:15], s[26:27]
	v_cndmask_b32_e64 v121, v121, 0, s[40:41]
	v_cndmask_b32_e64 v120, v120, 0, s[40:41]
	v_cndmask_b32_e64 v141, 0, v177, s[38:39]
	v_cndmask_b32_e64 v142, 0, v176, s[38:39]
	v_cndmask_b32_e64 v145, 0, v175, s[38:39]
	v_cndmask_b32_e64 v146, 0, v174, s[38:39]
	v_cndmask_b32_e64 v139, 0, v179, s[38:39]
	v_cndmask_b32_e64 v140, 0, v178, s[38:39]
	global_load_dwordx2 v[92:93], v[86:87], off
	global_load_dwordx2 v[90:91], v[84:85], off
	s_cmp_ge_i32 s13, s12
	s_cselect_b64 s[14:15], -1, 0
	v_lshlrev_b32_e32 v104, 16, v125
	v_and_b32_e32 v105, 0xffff0000, v125
	v_fma_f32 v94, |v104|, s33, 1.0
	v_rcp_f32_e32 v106, v94
	v_fma_f32 v94, |v105|, s33, 1.0
	v_rcp_f32_e32 v107, v94
	v_pk_mul_f32 v[108:109], v[104:105], v[104:105]
	v_cmp_gt_f32_e64 s[38:39], 0, v104
	v_mul_f32_e32 v94, 0xbf38aa3b, v108
	v_exp_f32_e32 v108, v94
	v_mov_b64_e32 v[94:95], s[86:87]
	v_pk_fma_f32 v[110:111], v[106:107], s[82:83], v[94:95] op_sel_hi:[1,0,0]
	v_mul_f32_e32 v109, 0xbf38aa3b, v109
	v_pk_fma_f32 v[110:111], v[106:107], v[110:111], s[96:97] op_sel_hi:[1,1,0]
	v_exp_f32_e32 v109, v109
	v_pk_fma_f32 v[110:111], v[106:107], v[110:111], s[30:31] op_sel_hi:[1,1,0]
	v_cmp_gt_f32_e64 s[40:41], 0, v105
	v_pk_fma_f32 v[110:111], v[106:107], v[110:111], s[36:37] op_sel_hi:[1,1,0]
	s_cmp_lt_i32 s13, s2
	v_pk_mul_f32 v[106:107], v[106:107], v[110:111]
	s_cselect_b64 s[12:13], -1, 0
	v_pk_mul_f32 v[106:107], v[108:109], v[106:107]
	s_mov_b32 s28, 0x358637bd
	v_pk_mul_f32 v[108:109], v[106:107], v[104:105]
	v_pk_fma_f32 v[104:105], v[106:107], v[104:105], v[104:105] neg_lo:[1,0,0] neg_hi:[1,0,0]
	s_mov_b32 s2, 0x3b800000
	v_cndmask_b32_e64 v111, v105, v109, s[40:41]
	v_cndmask_b32_e64 v110, v104, v108, s[38:39]
	v_lshlrev_b32_e32 v104, 16, v124
	v_and_b32_e32 v105, 0xffff0000, v124
	v_fma_f32 v106, |v104|, s33, 1.0
	v_fma_f32 v107, |v105|, s33, 1.0
	v_rcp_f32_e32 v106, v106
	v_rcp_f32_e32 v107, v107
	v_pk_mul_f32 v[108:109], v[104:105], v[104:105]
	v_cmp_gt_f32_e64 s[38:39], 0, v104
	v_mul_f32_e32 v108, 0xbf38aa3b, v108
	v_pk_fma_f32 v[114:115], v[106:107], s[82:83], v[94:95] op_sel_hi:[1,0,0]
	v_mul_f32_e32 v109, 0xbf38aa3b, v109
	v_exp_f32_e32 v108, v108
	v_pk_fma_f32 v[114:115], v[106:107], v[114:115], s[96:97] op_sel_hi:[1,1,0]
	v_exp_f32_e32 v109, v109
	v_pk_fma_f32 v[114:115], v[106:107], v[114:115], s[30:31] op_sel_hi:[1,1,0]
	v_cmp_gt_f32_e64 s[40:41], 0, v105
	v_pk_fma_f32 v[114:115], v[106:107], v[114:115], s[36:37] op_sel_hi:[1,1,0]
	v_readlane_b32 s26, v253, 48
	v_pk_mul_f32 v[106:107], v[106:107], v[114:115]
	v_readlane_b32 s27, v253, 49
	v_pk_mul_f32 v[106:107], v[108:109], v[106:107]
	v_lshlrev_b32_e32 v112, 16, v112
	v_pk_mul_f32 v[108:109], v[106:107], v[104:105]
	v_pk_fma_f32 v[104:105], v[106:107], v[104:105], v[104:105] neg_lo:[1,0,0] neg_hi:[1,0,0]
	v_mov_b32_e32 v107, v111
	v_cndmask_b32_e64 v114, v104, v108, s[38:39]
	v_lshlrev_b32_e32 v108, 16, v122
	v_cndmask_b32_e64 v115, v105, v109, s[40:41]
	v_fma_f32 v109, |v108|, s33, 1.0
	v_mov_b32_e32 v106, v115
	v_rcp_f32_e32 v109, v109
	v_mov_b32_e32 v104, v114
	v_mov_b32_e32 v105, v110
	v_pk_mul_f32 v[106:107], v[106:107], v[106:107]
	v_cmp_gt_f32_e64 s[38:39], 0, v108
	v_pk_fma_f32 v[104:105], v[104:105], v[104:105], v[106:107]
	s_nop 0
	v_add_f32_e32 v124, v104, v105
	v_mul_f32_e32 v105, v108, v108
	v_fmamk_f32 v104, v109, 0x3f07dc22, v199
	v_mul_f32_e32 v105, 0xbf38aa3b, v105
	v_fmaak_f32 v104, v109, v104, 0x3f35f0e3
	v_exp_f32_e32 v105, v105
	v_fmaak_f32 v104, v109, v104, 0xbe11a98e
	v_fmaak_f32 v104, v109, v104, 0x3e027906
	v_mul_f32_e32 v104, v109, v104
	v_mul_f32_e32 v104, v105, v104
	v_and_b32_e32 v105, 0xffff0000, v122
	v_fma_f32 v106, |v105|, s33, 1.0
	v_rcp_f32_e32 v106, v106
	v_mul_f32_e32 v107, v105, v105
	v_mul_f32_e32 v143, v104, v108
	v_fma_f32 v144, -v104, v108, v108
	v_fmamk_f32 v104, v106, 0x3f07dc22, v199
	v_mul_f32_e32 v107, 0xbf38aa3b, v107
	v_fmaak_f32 v104, v106, v104, 0x3f35f0e3
	v_exp_f32_e32 v107, v107
	v_fmaak_f32 v104, v106, v104, 0xbe11a98e
	v_fmaak_f32 v104, v106, v104, 0x3e027906
	v_mul_f32_e32 v104, v106, v104
	v_mul_f32_e32 v104, v107, v104
	v_mul_f32_e32 v147, v104, v105
	v_cmp_gt_f32_e64 s[40:41], 0, v105
	v_fma_f32 v148, -v104, v105, v105
	v_lshlrev_b32_e32 v104, 16, v123
	v_and_b32_e32 v105, 0xffff0000, v123
	v_fma_f32 v106, |v104|, s33, 1.0
	v_fma_f32 v107, |v105|, s33, 1.0
	v_rcp_f32_e32 v106, v106
	v_rcp_f32_e32 v107, v107
	v_pk_mul_f32 v[108:109], v[104:105], v[104:105]
	v_cmp_gt_f32_e64 s[42:43], 0, v104
	v_mul_f32_e32 v108, 0xbf38aa3b, v108
	v_pk_fma_f32 v[122:123], v[106:107], s[82:83], v[94:95] op_sel_hi:[1,0,0]
	v_mul_f32_e32 v109, 0xbf38aa3b, v109
	v_exp_f32_e32 v108, v108
	v_pk_fma_f32 v[122:123], v[106:107], v[122:123], s[96:97] op_sel_hi:[1,1,0]
	v_exp_f32_e32 v109, v109
	v_pk_fma_f32 v[122:123], v[106:107], v[122:123], s[30:31] op_sel_hi:[1,1,0]
	v_cmp_gt_f32_e64 s[46:47], 0, v105
	v_pk_fma_f32 v[122:123], v[106:107], v[122:123], s[36:37] op_sel_hi:[1,1,0]
	s_nop 1
	v_mov_b32_dpp v125, v124 quad_perm:[1,0,3,2] row_mask:0xf bank_mask:0xf
	v_pk_mul_f32 v[106:107], v[106:107], v[122:123]
	s_nop 0
	v_pk_mul_f32 v[106:107], v[108:109], v[106:107]
	s_nop 0
	v_pk_mul_f32 v[108:109], v[106:107], v[104:105]
	v_pk_fma_f32 v[104:105], v[106:107], v[104:105], v[104:105] neg_lo:[1,0,0] neg_hi:[1,0,0]
	v_cndmask_b32_e64 v106, v144, v143, s[38:39]
	v_cndmask_b32_e64 v105, v105, v109, s[46:47]
	v_cndmask_b32_e64 v104, v104, v108, s[42:43]
	v_cndmask_b32_e64 v108, v148, v147, s[40:41]
	v_mov_b32_e32 v109, v105
	v_mov_b32_e32 v107, v104
	v_pk_mul_f32 v[122:123], v[108:109], v[108:109]
	s_and_b64 s[38:39], s[14:15], s[12:13]
	v_pk_fma_f32 v[122:123], v[106:107], v[106:107], v[122:123]
	v_cndmask_b32_e64 v150, 0, v102, s[38:39]
	v_add_f32_e32 v107, v122, v123
	s_nop 1
	v_mov_b32_dpp v109, v107 quad_perm:[1,0,3,2] row_mask:0xf bank_mask:0xf
	s_waitcnt lgkmcnt(0)
	v_add_f32_e32 v122, v124, v125
	s_nop 1
	v_mov_b32_dpp v123, v122 quad_perm:[2,3,0,1] row_mask:0xf bank_mask:0xf
	v_cndmask_b32_e64 v149, 0, v103, s[38:39]
	v_cndmask_b32_e64 v148, 0, v100, s[38:39]
	s_waitcnt lgkmcnt(0)
	v_add_f32_e32 v107, v107, v109
	s_nop 1
	v_mov_b32_dpp v109, v107 quad_perm:[2,3,0,1] row_mask:0xf bank_mask:0xf
	s_waitcnt lgkmcnt(0)
	v_add_f32_e32 v122, v122, v123
	s_nop 1
	v_mov_b32_dpp v123, v122 row_half_mirror row_mask:0xf bank_mask:0xf
	v_cndmask_b32_e64 v147, 0, v101, s[38:39]
	v_cndmask_b32_e64 v144, 0, v98, s[38:39]
	s_waitcnt lgkmcnt(0)
	v_add_f32_e32 v107, v107, v109
	s_nop 1
	v_mov_b32_dpp v109, v107 row_half_mirror row_mask:0xf bank_mask:0xf
	s_waitcnt lgkmcnt(0)
	v_add_f32_e32 v122, v122, v123
	s_nop 1
	v_mov_b32_dpp v123, v122 row_mirror row_mask:0xf bank_mask:0xf
	v_cndmask_b32_e64 v143, 0, v99, s[38:39]
	v_lshlrev_b32_e32 v124, 16, v165
	s_waitcnt lgkmcnt(0)
	v_add_f32_e32 v102, v107, v109
	s_nop 1
	v_mov_b32_dpp v103, v102 row_mirror row_mask:0xf bank_mask:0xf
	s_waitcnt lgkmcnt(0)
	v_add_f32_e32 v107, v122, v123
	ds_swizzle_b32 v109, v107 offset:swizzle(SWAP,16)
	v_and_b32_e32 v125, 0xffff0000, v165
	s_lshl_b64 s[12:13], s[70:71], 8
	s_waitcnt lgkmcnt(0)
	v_add_f32_e32 v100, v102, v103
	ds_swizzle_b32 v102, v100 offset:swizzle(SWAP,16)
	s_waitcnt lgkmcnt(0)
	v_add_f32_e32 v101, v107, v109
	v_mov_b32_e32 v103, v101
	s_nop 1
	v_permlane32_swap_b32_e32 v101, v103
	s_waitcnt lgkmcnt(0)
	v_add_f32_e32 v100, v100, v102
	v_mov_b32_e32 v102, v100
	s_nop 1
	v_permlane32_swap_b32_e32 v100, v102
	v_pk_add_f32 v[102:103], v[100:101], v[102:103]
	v_mov_b64_e32 v[100:101], s[28:29]
	v_pk_fma_f32 v[102:103], v[102:103], s[2:3], v[100:101] op_sel_hi:[1,0,0]
	v_readlane_b32 s14, v253, 36
	v_mul_f32_e32 v107, 0x4b800000, v103
	v_cmp_gt_f32_e64 s[40:41], s35, v103
	v_cmp_gt_f32_e64 s[38:39], s35, v102
	v_readlane_b32 s15, v253, 37
	v_cndmask_b32_e64 v103, v103, v107, s[40:41]
	v_rsq_f32_e32 v103, v103
	s_nop 0
	v_mul_f32_e32 v98, 0x45800000, v103
	v_cndmask_b32_e64 v98, v103, v98, s[40:41]
	v_mul_f32_e32 v103, 0x4b800000, v102
	v_cndmask_b32_e64 v102, v102, v103, s[38:39]
	v_rsq_f32_e32 v107, v102
	s_waitcnt vmcnt(1)
	v_lshlrev_b32_e32 v102, 16, v92
	v_fma_f32 v103, |v102|, s33, 1.0
	v_pk_mul_f32 v[114:115], v[98:99], v[114:115] op_sel_hi:[0,1]
	v_pk_mul_f32 v[98:99], v[98:99], v[110:111] op_sel_hi:[0,1]
	v_rcp_f32_e32 v103, v103
	v_pk_mul_f32 v[114:115], v[60:61], v[114:115]
	v_pk_mul_f32 v[98:99], v[62:63], v[98:99]
	v_cvt_pk_bf16_f32 v114, v114, v115
	v_cvt_pk_bf16_f32 v115, v98, v99
	global_store_dwordx2 v[96:97], v[114:115], off
	v_mul_f32_e32 v97, v102, v102
	v_fmamk_f32 v96, v103, 0x3f07dc22, v199
	v_mul_f32_e32 v97, 0xbf38aa3b, v97
	v_fmaak_f32 v96, v103, v96, 0x3f35f0e3
	v_exp_f32_e32 v97, v97
	v_fmaak_f32 v96, v103, v96, 0xbe11a98e
	v_fmaak_f32 v96, v103, v96, 0x3e027906
	v_mul_f32_e32 v96, v103, v96
	v_and_b32_e32 v92, 0xffff0000, v92
	v_mul_f32_e32 v96, v97, v96
	v_fma_f32 v97, |v92|, s33, 1.0
	v_rcp_f32_e32 v97, v97
	v_mul_f32_e32 v98, v92, v92
	v_mul_f32_e32 v110, v96, v102
	v_fma_f32 v111, -v96, v102, v102
	v_fmamk_f32 v96, v97, 0x3f07dc22, v199
	v_mul_f32_e32 v98, 0xbf38aa3b, v98
	v_fmaak_f32 v96, v97, v96, 0x3f35f0e3
	v_exp_f32_e32 v98, v98
	v_fmaak_f32 v96, v97, v96, 0xbe11a98e
	v_fmaak_f32 v96, v97, v96, 0x3e027906
	v_mul_f32_e32 v96, v97, v96
	v_mul_f32_e32 v96, v98, v96
	v_mul_f32_e32 v114, v96, v92
	v_cmp_gt_f32_e64 s[42:43], 0, v92
	v_fma_f32 v115, -v96, v92, v92
	v_lshlrev_b32_e32 v92, 16, v93
	v_and_b32_e32 v93, 0xffff0000, v93
	v_fma_f32 v96, |v92|, s33, 1.0
	v_fma_f32 v97, |v93|, s33, 1.0
	v_rcp_f32_e32 v96, v96
	v_rcp_f32_e32 v97, v97
	v_pk_mul_f32 v[98:99], v[92:93], v[92:93]
	v_cmp_gt_f32_e64 s[40:41], 0, v102
	v_mul_f32_e32 v98, 0xbf38aa3b, v98
	v_pk_fma_f32 v[102:103], v[96:97], s[82:83], v[94:95] op_sel_hi:[1,0,0]
	v_mul_f32_e32 v99, 0xbf38aa3b, v99
	v_exp_f32_e32 v98, v98
	v_pk_fma_f32 v[102:103], v[96:97], v[102:103], s[96:97] op_sel_hi:[1,1,0]
	v_exp_f32_e32 v99, v99
	v_pk_fma_f32 v[102:103], v[96:97], v[102:103], s[30:31] op_sel_hi:[1,1,0]
	v_cmp_gt_f32_e64 s[46:47], 0, v92
	v_pk_fma_f32 v[102:103], v[96:97], v[102:103], s[36:37] op_sel_hi:[1,1,0]
	v_cmp_gt_f32_e64 s[48:49], 0, v93
	v_pk_mul_f32 v[96:97], v[96:97], v[102:103]
	v_mul_f32_e32 v109, 0x45800000, v107
	v_pk_mul_f32 v[96:97], v[98:99], v[96:97]
	s_nop 0
	v_pk_mul_f32 v[98:99], v[96:97], v[92:93]
	v_pk_fma_f32 v[92:93], v[96:97], v[92:93], v[92:93] neg_lo:[1,0,0] neg_hi:[1,0,0]
	v_cndmask_b32_e64 v96, v111, v110, s[40:41]
	v_cndmask_b32_e64 v93, v93, v99, s[48:49]
	v_cndmask_b32_e64 v92, v92, v98, s[46:47]
	v_cndmask_b32_e64 v98, v115, v114, s[42:43]
	v_mov_b32_e32 v99, v93
	v_pk_mul_f32 v[102:103], v[98:99], v[98:99]
	s_waitcnt vmcnt(1)
	v_lshlrev_b32_e32 v99, 16, v90
	v_fma_f32 v110, |v99|, s33, 1.0
	v_rcp_f32_e32 v110, v110
	v_mov_b32_e32 v97, v92
	v_pk_fma_f32 v[102:103], v[96:97], v[96:97], v[102:103]
	v_and_b32_e32 v90, 0xffff0000, v90
	v_add_f32_e32 v97, v102, v103
	v_mul_f32_e32 v103, v99, v99
	v_fmamk_f32 v102, v110, 0x3f07dc22, v199
	v_mul_f32_e32 v103, 0xbf38aa3b, v103
	v_fmaak_f32 v102, v110, v102, 0x3f35f0e3
	v_exp_f32_e32 v103, v103
	v_fmaak_f32 v102, v110, v102, 0xbe11a98e
	v_fmaak_f32 v102, v110, v102, 0x3e027906
	v_mul_f32_e32 v102, v110, v102
	v_mul_f32_e32 v102, v103, v102
	v_fma_f32 v103, |v90|, s33, 1.0
	v_rcp_f32_e32 v103, v103
	v_mul_f32_e32 v110, v90, v90
	v_mul_f32_e32 v115, v102, v99
	v_cmp_gt_f32_e64 s[40:41], 0, v99
	v_fma_f32 v99, -v102, v99, v99
	v_fmamk_f32 v102, v103, 0x3f07dc22, v199
	v_mul_f32_e32 v110, 0xbf38aa3b, v110
	v_fmaak_f32 v102, v103, v102, 0x3f35f0e3
	v_exp_f32_e32 v110, v110
	v_fmaak_f32 v102, v103, v102, 0xbe11a98e
	v_fmaak_f32 v102, v103, v102, 0x3e027906
	v_mul_f32_e32 v102, v103, v102
	v_mul_f32_e32 v102, v110, v102
	v_mul_f32_e32 v122, v102, v90
	v_cmp_gt_f32_e64 s[42:43], 0, v90
	v_fma_f32 v123, -v102, v90, v90
	v_lshlrev_b32_e32 v90, 16, v91
	v_and_b32_e32 v91, 0xffff0000, v91
	v_fma_f32 v102, |v90|, s33, 1.0
	v_fma_f32 v103, |v91|, s33, 1.0
	v_rcp_f32_e32 v102, v102
	v_rcp_f32_e32 v103, v103
	v_pk_mul_f32 v[110:111], v[90:91], v[90:91]
	v_cmp_gt_f32_e64 s[46:47], 0, v90
	v_mul_f32_e32 v110, 0xbf38aa3b, v110
	v_pk_fma_f32 v[94:95], v[102:103], s[82:83], v[94:95] op_sel_hi:[1,0,0]
	v_mul_f32_e32 v111, 0xbf38aa3b, v111
	v_exp_f32_e32 v110, v110
	v_pk_fma_f32 v[94:95], v[102:103], v[94:95], s[96:97] op_sel_hi:[1,1,0]
	v_exp_f32_e32 v111, v111
	v_pk_fma_f32 v[94:95], v[102:103], v[94:95], s[30:31] op_sel_hi:[1,1,0]
	v_cmp_gt_f32_e64 s[48:49], 0, v91
	v_pk_fma_f32 v[94:95], v[102:103], v[94:95], s[36:37] op_sel_hi:[1,1,0]
	s_nop 1
	v_mov_b32_dpp v114, v97 quad_perm:[1,0,3,2] row_mask:0xf bank_mask:0xf
	v_pk_mul_f32 v[94:95], v[102:103], v[94:95]
	s_waitcnt lgkmcnt(0)
	v_add_f32_e32 v97, v97, v114
	v_pk_mul_f32 v[94:95], v[110:111], v[94:95]
	v_lshlrev_b32_e32 v114, 16, v160
	v_pk_mul_f32 v[102:103], v[94:95], v[90:91]
	v_pk_fma_f32 v[90:91], v[94:95], v[90:91], v[90:91] neg_lo:[1,0,0] neg_hi:[1,0,0]
	v_cndmask_b32_e64 v94, v99, v115, s[40:41]
	v_cndmask_b32_e64 v91, v91, v103, s[48:49]
	v_cndmask_b32_e64 v90, v90, v102, s[46:47]
	v_cndmask_b32_e64 v102, v123, v122, s[42:43]
	v_mov_b32_e32 v103, v91
	v_mov_b32_e32 v95, v90
	v_pk_mul_f32 v[110:111], v[102:103], v[102:103]
	s_nop 1
	v_mov_b32_dpp v103, v97 quad_perm:[2,3,0,1] row_mask:0xf bank_mask:0xf
	v_pk_fma_f32 v[110:111], v[94:95], v[94:95], v[110:111]
	v_lshlrev_b32_e32 v122, 16, v166
	v_add_f32_e32 v95, v110, v111
	s_nop 1
	v_mov_b32_dpp v99, v95 quad_perm:[1,0,3,2] row_mask:0xf bank_mask:0xf
	s_waitcnt lgkmcnt(0)
	v_add_f32_e32 v97, v97, v103
	s_nop 1
	v_mov_b32_dpp v103, v97 row_half_mirror row_mask:0xf bank_mask:0xf
	v_cndmask_b32_e64 v110, v107, v109, s[38:39]
	v_mov_b32_e32 v111, v108
	s_waitcnt lgkmcnt(0)
	v_add_f32_e32 v95, v95, v99
	s_nop 1
	v_mov_b32_dpp v99, v95 quad_perm:[2,3,0,1] row_mask:0xf bank_mask:0xf
	s_waitcnt lgkmcnt(0)
	v_add_f32_e32 v97, v97, v103
	s_nop 1
	v_mov_b32_dpp v103, v97 row_mirror row_mask:0xf bank_mask:0xf
	v_mov_b32_e32 v107, v110
	v_pk_mul_f32 v[106:107], v[110:111], v[106:107]
	s_waitcnt lgkmcnt(0)
	v_add_f32_e32 v95, v95, v99
	s_nop 1
	v_mov_b32_dpp v99, v95 row_half_mirror row_mask:0xf bank_mask:0xf
	s_waitcnt lgkmcnt(0)
	v_add_f32_e32 v97, v97, v103
	ds_swizzle_b32 v103, v97 offset:swizzle(SWAP,16)
	v_pk_mul_f32 v[104:105], v[104:105], v[110:111] op_sel_hi:[1,0]
	v_pk_mul_f32 v[106:107], v[60:61], v[106:107]
	s_waitcnt lgkmcnt(0)
	v_add_f32_e32 v95, v95, v99
	s_nop 1
	v_mov_b32_dpp v99, v95 row_mirror row_mask:0xf bank_mask:0xf
	s_waitcnt lgkmcnt(0)
	v_add_f32_e32 v109, v97, v103
	v_mov_b32_e32 v111, v109
	s_nop 1
	v_permlane32_swap_b32_e32 v109, v111
	s_waitcnt lgkmcnt(0)
	v_add_f32_e32 v95, v95, v99
	ds_swizzle_b32 v99, v95 offset:swizzle(SWAP,16)
	v_pk_mul_f32 v[104:105], v[62:63], v[104:105]
	v_cvt_pk_bf16_f32 v106, v106, v107
	v_cvt_pk_bf16_f32 v107, v104, v105
	global_store_dwordx2 v[88:89], v[106:107], off
	s_waitcnt lgkmcnt(0)
	v_add_f32_e32 v108, v95, v99
	v_mov_b32_e32 v110, v108
	s_nop 1
	v_permlane32_swap_b32_e32 v108, v110
	v_pk_add_f32 v[108:109], v[108:109], v[110:111]
	v_mov_b32_e32 v89, v98
	v_pk_fma_f32 v[100:101], v[108:109], s[2:3], v[100:101] op_sel_hi:[1,0,0]
	v_and_b32_e32 v123, 0xffff0000, v166
	v_mul_f32_e32 v95, 0x4b800000, v101
	v_cmp_gt_f32_e64 s[38:39], s35, v101
	v_cmp_gt_f32_e64 s[40:41], s35, v100
	v_lshlrev_b32_e32 v108, 16, v164
	v_cndmask_b32_e64 v95, v101, v95, s[38:39]
	v_rsq_f32_e32 v95, v95
	v_and_b32_e32 v109, 0xffff0000, v164
	v_lshlrev_b32_e32 v110, 16, v161
	v_and_b32_e32 v111, 0xffff0000, v161
	v_mul_f32_e32 v88, 0x45800000, v95
	v_cndmask_b32_e64 v88, v95, v88, s[38:39]
	v_mov_b32_e32 v97, v88
	v_pk_mul_f32 v[96:97], v[88:89], v[96:97]
	v_pk_mul_f32 v[88:89], v[92:93], v[88:89] op_sel_hi:[1,0]
	v_mul_f32_e32 v92, 0x4b800000, v100
	v_cndmask_b32_e64 v92, v100, v92, s[40:41]
	v_rsq_f32_e32 v92, v92
	v_pk_mul_f32 v[96:97], v[60:61], v[96:97]
	v_pk_mul_f32 v[88:89], v[62:63], v[88:89]
	v_cvt_pk_bf16_f32 v96, v96, v97
	v_cvt_pk_bf16_f32 v97, v88, v89
	global_store_dwordx2 v[86:87], v[96:97], off
	v_mul_f32_e32 v86, 0x45800000, v92
	v_cndmask_b32_e64 v86, v92, v86, s[40:41]
	v_mov_b32_e32 v87, v102
	v_mov_b32_e32 v95, v86
	v_pk_mul_f32 v[88:89], v[86:87], v[94:95]
	v_pk_mul_f32 v[86:87], v[90:91], v[86:87] op_sel_hi:[1,0]
	v_pk_mul_f32 v[88:89], v[60:61], v[88:89]
	v_pk_mul_f32 v[86:87], v[62:63], v[86:87]
	v_cvt_pk_bf16_f32 v88, v88, v89
	v_cvt_pk_bf16_f32 v89, v86, v87
	global_store_dwordx2 v[84:85], v[88:89], off
	v_lshlrev_b32_e32 v84, 16, v168
	v_and_b32_e32 v85, 0xffff0000, v168
	v_lshlrev_b32_e32 v86, 16, v167
	v_and_b32_e32 v87, 0xffff0000, v167
	v_pk_fma_f32 v[86:87], v[2:3], v[86:87], 0 op_sel_hi:[1,1,0]
	v_pk_fma_f32 v[84:85], v[0:1], v[84:85], 0 op_sel_hi:[1,1,0]
	v_pk_fma_f32 v[86:87], v[14:15], v[124:125], v[86:87]
	v_pk_fma_f32 v[84:85], v[12:13], v[122:123], v[84:85]
	v_pk_fma_f32 v[88:89], v[22:23], v[110:111], v[86:87]
	v_pk_fma_f32 v[90:91], v[20:21], v[108:109], v[84:85]
	v_lshlrev_b32_e32 v84, 16, v163
	v_and_b32_e32 v85, 0xffff0000, v163
	v_lshlrev_b32_e32 v86, 16, v117
	v_and_b32_e32 v87, 0xffff0000, v117
	v_pk_fma_f32 v[92:93], v[32:33], v[84:85], v[90:91]
	v_pk_fma_f32 v[94:95], v[34:35], v[86:87], v[88:89]
	v_lshlrev_b32_e32 v88, 16, v162
	v_and_b32_e32 v89, 0xffff0000, v162
	v_pk_fma_f32 v[162:163], v[48:49], v[88:89], v[92:93]
	v_lshlrev_b32_e32 v90, 16, v116
	v_mul_f32_e32 v92, 0xbfb8aa3b, v162
	v_exp_f32_e32 v92, v92
	v_mul_f32_e32 v93, 0xbfb8aa3b, v163
	v_exp_f32_e32 v93, v93
	v_and_b32_e32 v91, 0xffff0000, v116
	v_pk_fma_f32 v[164:165], v[50:51], v[90:91], v[94:95]
	v_add_f32_e32 v92, 1.0, v92
	v_rcp_f32_e32 v166, v92
	v_add_f32_e32 v92, 1.0, v93
	v_mul_f32_e32 v93, 0xbfb8aa3b, v164
	v_exp_f32_e32 v93, v93
	v_mul_f32_e32 v94, 0xbfb8aa3b, v165
	v_exp_f32_e32 v94, v94
	v_rcp_f32_e32 v167, v92
	v_add_f32_e32 v92, 1.0, v93
	v_rcp_f32_e32 v168, v92
	v_add_f32_e32 v92, 1.0, v94
	v_rcp_f32_e32 v169, v92
	v_lshlrev_b32_e32 v92, 16, v130
	v_and_b32_e32 v93, 0xffff0000, v130
	v_lshlrev_b32_e32 v94, 16, v128
	v_and_b32_e32 v95, 0xffff0000, v128
	v_pk_fma_f32 v[94:95], v[6:7], v[94:95], 0 op_sel_hi:[1,1,0]
	v_pk_fma_f32 v[92:93], v[4:5], v[92:93], 0 op_sel_hi:[1,1,0]
	v_lshlrev_b32_e32 v128, 16, v129
	v_and_b32_e32 v129, 0xffff0000, v129
	v_lshlrev_b32_e32 v130, 16, v131
	v_and_b32_e32 v131, 0xffff0000, v131
	v_pk_fma_f32 v[92:93], v[24:25], v[128:129], v[92:93]
	v_pk_fma_f32 v[94:95], v[26:27], v[130:131], v[94:95]
	v_and_b32_e32 v115, 0xffff0000, v160
	v_lshlrev_b32_e32 v116, 16, v157
	v_and_b32_e32 v117, 0xffff0000, v157
	v_pk_fma_f32 v[96:97], v[46:47], v[116:117], v[94:95]
	v_pk_fma_f32 v[98:99], v[44:45], v[114:115], v[92:93]
	v_lshlrev_b32_e32 v92, 16, v159
	v_and_b32_e32 v93, 0xffff0000, v159
	v_lshlrev_b32_e32 v94, 16, v119
	v_and_b32_e32 v95, 0xffff0000, v119
	v_pk_fma_f32 v[100:101], v[36:37], v[92:93], v[98:99]
	v_pk_fma_f32 v[102:103], v[38:39], v[94:95], v[96:97]
	v_lshlrev_b32_e32 v96, 16, v158
	v_and_b32_e32 v97, 0xffff0000, v158
	v_pk_fma_f32 v[158:159], v[52:53], v[96:97], v[100:101]
	v_lshlrev_b32_e32 v98, 16, v118
	v_mul_f32_e32 v100, 0xbfb8aa3b, v158
	v_exp_f32_e32 v100, v100
	v_mul_f32_e32 v101, 0xbfb8aa3b, v159
	v_exp_f32_e32 v101, v101
	v_and_b32_e32 v99, 0xffff0000, v118
	v_pk_fma_f32 v[160:161], v[54:55], v[98:99], v[102:103]
	v_add_f32_e32 v100, 1.0, v100
	v_rcp_f32_e32 v170, v100
	v_add_f32_e32 v100, 1.0, v101
	v_mul_f32_e32 v101, 0xbfb8aa3b, v160
	v_exp_f32_e32 v101, v101
	v_mul_f32_e32 v102, 0xbfb8aa3b, v161
	v_exp_f32_e32 v102, v102
	v_rcp_f32_e32 v171, v100
	v_add_f32_e32 v100, 1.0, v101
	v_rcp_f32_e32 v172, v100
	v_add_f32_e32 v100, 1.0, v102
	v_rcp_f32_e32 v173, v100
	v_pk_mul_f32 v[164:165], v[164:165], v[168:169]
	v_pk_mul_f32 v[162:163], v[162:163], v[166:167]
	v_mov_b32_e32 v169, v165
	v_mov_b32_e32 v168, v163
	v_pk_mul_f32 v[160:161], v[160:161], v[172:173]
	v_pk_mul_f32 v[158:159], v[158:159], v[170:171]
	v_mov_b32_e32 v166, v162
	v_mov_b32_e32 v167, v164
	v_pk_mul_f32 v[168:169], v[168:169], v[168:169]
	v_mov_b32_e32 v170, v159
	v_mov_b32_e32 v171, v161
	v_pk_fma_f32 v[166:167], v[166:167], v[166:167], v[168:169]
	v_mov_b32_e32 v168, v158
	v_mov_b32_e32 v169, v160
	v_pk_mul_f32 v[170:171], v[170:171], v[170:171]
	v_lshlrev_b32_e32 v100, 16, v136
	v_pk_fma_f32 v[168:169], v[168:169], v[168:169], v[170:171]
	v_mov_b32_e32 v171, v166
	v_mov_b32_e32 v170, v168
	v_mov_b32_e32 v166, v169
	v_pk_add_f32 v[166:167], v[170:171], v[166:167]
	s_nop 1
	v_mov_b32_dpp v169, v167 quad_perm:[1,0,3,2] row_mask:0xf bank_mask:0xf
	s_nop 1
	v_mov_b32_dpp v168, v166 quad_perm:[1,0,3,2] row_mask:0xf bank_mask:0xf
	v_and_b32_e32 v101, 0xffff0000, v136
	v_lshlrev_b32_e32 v102, 16, v134
	v_and_b32_e32 v103, 0xffff0000, v134
	v_pk_fma_f32 v[102:103], v[10:11], v[102:103], 0 op_sel_hi:[1,1,0]
	s_waitcnt lgkmcnt(0)
	v_pk_add_f32 v[166:167], v[166:167], v[168:169]
	v_pk_fma_f32 v[100:101], v[8:9], v[100:101], 0 op_sel_hi:[1,1,0]
	v_lshlrev_b32_e32 v134, 16, v135
	v_and_b32_e32 v135, 0xffff0000, v135
	v_lshlrev_b32_e32 v136, 16, v137
	v_and_b32_e32 v137, 0xffff0000, v137
	s_nop 1
	v_mov_b32_dpp v169, v167 quad_perm:[2,3,0,1] row_mask:0xf bank_mask:0xf
	s_nop 1
	v_mov_b32_dpp v168, v166 quad_perm:[2,3,0,1] row_mask:0xf bank_mask:0xf
	v_pk_fma_f32 v[100:101], v[16:17], v[134:135], v[100:101]
	v_pk_fma_f32 v[102:103], v[18:19], v[136:137], v[102:103]
	v_lshlrev_b32_e32 v118, 16, v120
	v_and_b32_e32 v119, 0xffff0000, v120
	v_lshlrev_b32_e32 v120, 16, v121
	v_and_b32_e32 v121, 0xffff0000, v121
	v_pk_fma_f32 v[104:105], v[30:31], v[120:121], v[102:103]
	v_pk_fma_f32 v[106:107], v[28:29], v[118:119], v[100:101]
	v_lshlrev_b32_e32 v100, 16, v156
	v_and_b32_e32 v101, 0xffff0000, v156
	v_lshlrev_b32_e32 v102, 16, v132
	v_and_b32_e32 v103, 0xffff0000, v132
	v_pk_fma_f32 v[156:157], v[40:41], v[100:101], v[106:107]
	v_pk_fma_f32 v[174:175], v[42:43], v[102:103], v[104:105]
	v_lshlrev_b32_e32 v104, 16, v155
	v_and_b32_e32 v105, 0xffff0000, v155
	v_pk_fma_f32 v[156:157], v[56:57], v[104:105], v[156:157]
	v_lshlrev_b32_e32 v106, 16, v126
	v_and_b32_e32 v107, 0xffff0000, v126
	v_mul_f32_e32 v126, 0xbfb8aa3b, v156
	s_waitcnt lgkmcnt(0)
	v_pk_add_f32 v[166:167], v[166:167], v[168:169]
	v_exp_f32_e32 v126, v126
	v_mul_f32_e32 v132, 0xbfb8aa3b, v157
	s_nop 1
	v_mov_b32_dpp v169, v167 row_half_mirror row_mask:0xf bank_mask:0xf
	s_nop 1
	v_mov_b32_dpp v168, v166 row_half_mirror row_mask:0xf bank_mask:0xf
	v_exp_f32_e32 v132, v132
	v_add_f32_e32 v126, 1.0, v126
	v_pk_fma_f32 v[174:175], v[58:59], v[106:107], v[174:175]
	v_rcp_f32_e32 v170, v126
	v_add_f32_e32 v126, 1.0, v132
	s_waitcnt lgkmcnt(0)
	v_pk_add_f32 v[166:167], v[166:167], v[168:169]
	v_rcp_f32_e32 v171, v126
	v_mul_f32_e32 v126, 0xbfb8aa3b, v174
	s_nop 1
	v_mov_b32_dpp v169, v167 row_mirror row_mask:0xf bank_mask:0xf
	s_nop 1
	v_mov_b32_dpp v168, v166 row_mirror row_mask:0xf bank_mask:0xf
	v_exp_f32_e32 v126, v126
	v_mul_f32_e32 v132, 0xbfb8aa3b, v175
	v_exp_f32_e32 v132, v132
	v_pk_mul_f32 v[156:157], v[156:157], v[170:171]
	v_add_f32_e32 v126, 1.0, v126
	s_waitcnt lgkmcnt(0)
	v_pk_add_f32 v[166:167], v[166:167], v[168:169]
	v_rcp_f32_e32 v172, v126
	v_add_f32_e32 v126, 1.0, v132
	v_pk_add_f32 v[166:167], v[166:167], s[28:29] op_sel_hi:[1,0]
	v_rcp_f32_e32 v173, v126
	v_mul_f32_e32 v126, 0x4b800000, v167
	v_cmp_gt_f32_e64 s[38:39], s35, v167
	v_cmp_gt_f32_e64 s[40:41], s35, v166
	v_pk_mul_f32 v[170:171], v[174:175], v[172:173]
	v_cndmask_b32_e64 v126, v167, v126, s[38:39]
	v_rsq_f32_e32 v126, v126
	v_lshl_add_u64 v[172:173], s[12:13], 0, v[64:65]
	v_pk_fma_f32 v[122:123], v[0:1], v[122:123], 0 op_sel_hi:[1,1,0]
	v_lshlrev_b64 v[168:169], 1, v[172:173]
	v_mul_f32_e32 v132, 0x45800000, v126
	v_cndmask_b32_e64 v126, v126, v132, s[38:39]
	v_mul_f32_e32 v132, 0x4b800000, v166
	v_cndmask_b32_e64 v132, v166, v132, s[40:41]
	v_rsq_f32_e32 v132, v132
	v_mul_f32_e32 v126, 0x3e000000, v126
	v_pk_mul_f32 v[162:163], v[162:163], v[126:127] op_sel_hi:[1,0]
	v_pk_mul_f32 v[164:165], v[164:165], v[126:127] op_sel_hi:[1,0]
	v_mul_f32_e32 v126, 0x45800000, v132
	v_cndmask_b32_e64 v126, v132, v126, s[40:41]
	v_pk_mul_f32 v[158:159], v[158:159], v[126:127] op_sel_hi:[1,0]
	v_pk_mul_f32 v[160:161], v[160:161], v[126:127] op_sel_hi:[1,0]
	v_pk_fma_f32 v[122:123], v[12:13], v[108:109], v[122:123]
	v_cvt_pk_bf16_f32 v158, v158, v159
	v_cvt_pk_bf16_f32 v159, v160, v161
	v_lshl_add_u64 v[160:161], s[14:15], 0, v[168:169]
	v_pk_fma_f32 v[122:123], v[20:21], v[84:85], v[122:123]
	global_store_dwordx2 v[160:161], v[158:159], off
	v_cvt_pk_bf16_f32 v156, v156, v157
	v_cvt_pk_bf16_f32 v157, v170, v171
	v_lshl_add_u64 v[158:159], s[26:27], 0, v[168:169]
	v_pk_fma_f32 v[122:123], v[32:33], v[88:89], v[122:123]
	v_lshlrev_b32_e32 v126, 16, v127
	v_and_b32_e32 v127, 0xffff0000, v127
	global_store_dwordx2 v[158:159], v[156:157], off
	v_pk_fma_f32 v[156:157], v[48:49], v[126:127], v[122:123]
	v_pk_fma_f32 v[124:125], v[2:3], v[124:125], 0 op_sel_hi:[1,1,0]
	v_mul_f32_e32 v122, 0xbfb8aa3b, v156
	v_exp_f32_e32 v122, v122
	v_mul_f32_e32 v123, 0xbfb8aa3b, v157
	v_pk_fma_f32 v[124:125], v[14:15], v[110:111], v[124:125]
	v_exp_f32_e32 v123, v123
	v_pk_fma_f32 v[124:125], v[22:23], v[86:87], v[124:125]
	v_lshlrev_b32_e32 v132, 16, v133
	v_pk_fma_f32 v[124:125], v[34:35], v[90:91], v[124:125]
	v_and_b32_e32 v133, 0xffff0000, v133
	v_pk_fma_f32 v[158:159], v[50:51], v[132:133], v[124:125]
	v_add_f32_e32 v122, 1.0, v122
	v_rcp_f32_e32 v160, v122
	v_add_f32_e32 v122, 1.0, v123
	v_mul_f32_e32 v123, 0xbfb8aa3b, v158
	v_exp_f32_e32 v123, v123
	v_mul_f32_e32 v124, 0xbfb8aa3b, v159
	v_exp_f32_e32 v124, v124
	v_lshl_add_u64 v[172:173], s[18:19], 0, v[168:169]
	v_cvt_pk_bf16_f32 v162, v162, v163
	v_cvt_pk_bf16_f32 v163, v164, v165
	v_rcp_f32_e32 v161, v122
	v_add_f32_e32 v122, 1.0, v123
	global_store_dwordx2 v[172:173], v[162:163], off
	v_rcp_f32_e32 v162, v122
	v_add_f32_e32 v122, 1.0, v124
	v_pk_fma_f32 v[124:125], v[4:5], v[128:129], 0 op_sel_hi:[1,1,0]
	v_rcp_f32_e32 v163, v122
	v_pk_fma_f32 v[124:125], v[24:25], v[114:115], v[124:125]
	v_pk_fma_f32 v[122:123], v[6:7], v[130:131], 0 op_sel_hi:[1,1,0]
	v_pk_fma_f32 v[124:125], v[44:45], v[92:93], v[124:125]
	v_pk_fma_f32 v[122:123], v[26:27], v[116:117], v[122:123]
	v_pk_fma_f32 v[128:129], v[36:37], v[96:97], v[124:125]
	v_lshlrev_b32_e32 v124, 16, v154
	v_and_b32_e32 v125, 0xffff0000, v154
	v_pk_fma_f32 v[154:155], v[52:53], v[124:125], v[128:129]
	v_pk_fma_f32 v[122:123], v[46:47], v[94:95], v[122:123]
	v_mul_f32_e32 v128, 0xbfb8aa3b, v154
	v_exp_f32_e32 v128, v128
	v_pk_fma_f32 v[122:123], v[38:39], v[98:99], v[122:123]
	v_lshlrev_b32_e32 v130, 16, v153
	v_and_b32_e32 v131, 0xffff0000, v153
	v_mul_f32_e32 v129, 0xbfb8aa3b, v155
	v_pk_fma_f32 v[164:165], v[54:55], v[130:131], v[122:123]
	v_exp_f32_e32 v129, v129
	v_mul_f32_e32 v123, 0xbfb8aa3b, v164
	v_add_f32_e32 v122, 1.0, v128
	v_exp_f32_e32 v123, v123
	v_mul_f32_e32 v128, 0xbfb8aa3b, v165
	v_exp_f32_e32 v128, v128
	v_rcp_f32_e32 v166, v122
	v_add_f32_e32 v122, 1.0, v129
	v_rcp_f32_e32 v167, v122
	v_add_f32_e32 v122, 1.0, v123
	v_rcp_f32_e32 v168, v122
	v_add_f32_e32 v122, 1.0, v128
	v_rcp_f32_e32 v169, v122
	v_pk_fma_f32 v[122:123], v[10:11], v[136:137], 0 op_sel_hi:[1,1,0]
	v_pk_fma_f32 v[128:129], v[8:9], v[134:135], 0 op_sel_hi:[1,1,0]
	v_pk_fma_f32 v[122:123], v[18:19], v[120:121], v[122:123]
	v_pk_fma_f32 v[128:129], v[16:17], v[118:119], v[128:129]
	v_pk_fma_f32 v[122:123], v[30:31], v[102:103], v[122:123]
	v_pk_fma_f32 v[128:129], v[28:29], v[100:101], v[128:129]
	v_pk_fma_f32 v[136:137], v[42:43], v[106:107], v[122:123]
	v_pk_fma_f32 v[134:135], v[40:41], v[104:105], v[128:129]
	v_lshlrev_b32_e32 v122, 16, v152
	v_and_b32_e32 v123, 0xffff0000, v152
	v_pk_fma_f32 v[134:135], v[56:57], v[122:123], v[134:135]
	v_pk_mul_f32 v[156:157], v[156:157], v[160:161]
	v_mul_f32_e32 v152, 0xbfb8aa3b, v135
	v_exp_f32_e32 v170, v152
	v_pk_mul_f32 v[152:153], v[158:159], v[162:163]
	v_mov_b32_e32 v160, v157
	v_mov_b32_e32 v161, v153
	v_mov_b32_e32 v158, v156
	v_mov_b32_e32 v159, v152
	v_pk_mul_f32 v[160:161], v[160:161], v[160:161]
	v_pk_mul_f32 v[154:155], v[154:155], v[166:167]
	v_pk_fma_f32 v[158:159], v[158:159], v[158:159], v[160:161]
	v_pk_mul_f32 v[160:161], v[164:165], v[168:169]
	v_mov_b32_e32 v164, v155
	v_mov_b32_e32 v165, v161
	v_mov_b32_e32 v162, v154
	v_mov_b32_e32 v163, v160
	v_pk_mul_f32 v[164:165], v[164:165], v[164:165]
	v_lshlrev_b32_e32 v128, 16, v151
	v_pk_fma_f32 v[162:163], v[162:163], v[162:163], v[164:165]
	v_mov_b32_e32 v165, v158
	v_mov_b32_e32 v164, v162
	v_mov_b32_e32 v158, v163
	v_pk_add_f32 v[158:159], v[164:165], v[158:159]
	s_nop 1
	v_mov_b32_dpp v163, v159 quad_perm:[1,0,3,2] row_mask:0xf bank_mask:0xf
	s_nop 1
	v_mov_b32_dpp v162, v158 quad_perm:[1,0,3,2] row_mask:0xf bank_mask:0xf
	v_and_b32_e32 v129, 0xffff0000, v151
	v_mul_f32_e32 v151, 0xbfb8aa3b, v134
	v_exp_f32_e32 v151, v151
	v_pk_fma_f32 v[136:137], v[58:59], v[128:129], v[136:137]
	s_waitcnt lgkmcnt(0)
	v_pk_add_f32 v[158:159], v[158:159], v[162:163]
	s_nop 1
	v_mov_b32_dpp v163, v159 quad_perm:[2,3,0,1] row_mask:0xf bank_mask:0xf
	s_nop 1
	v_mov_b32_dpp v162, v158 quad_perm:[2,3,0,1] row_mask:0xf bank_mask:0xf
	v_add_f32_e32 v151, 1.0, v151
	v_rcp_f32_e32 v164, v151
	v_add_f32_e32 v151, 1.0, v170
	v_rcp_f32_e32 v165, v151
	s_waitcnt lgkmcnt(0)
	v_pk_add_f32 v[158:159], v[158:159], v[162:163]
	s_nop 1
	v_mov_b32_dpp v163, v159 row_half_mirror row_mask:0xf bank_mask:0xf
	s_nop 1
	v_mov_b32_dpp v162, v158 row_half_mirror row_mask:0xf bank_mask:0xf
	v_mul_f32_e32 v151, 0xbfb8aa3b, v136
	v_exp_f32_e32 v151, v151
	v_mul_f32_e32 v166, 0xbfb8aa3b, v137
	v_exp_f32_e32 v167, v166
	s_waitcnt lgkmcnt(0)
	v_pk_add_f32 v[158:159], v[158:159], v[162:163]
	s_nop 1
	v_mov_b32_dpp v163, v159 row_mirror row_mask:0xf bank_mask:0xf
	s_nop 1
	v_mov_b32_dpp v162, v158 row_mirror row_mask:0xf bank_mask:0xf
	v_add_f32_e32 v151, 1.0, v151
	v_rcp_f32_e32 v166, v151
	v_add_f32_e32 v151, 1.0, v167
	v_rcp_f32_e32 v167, v151
	s_waitcnt lgkmcnt(0)
	v_pk_add_f32 v[158:159], v[158:159], v[162:163]
	s_lshl_b64 s[12:13], s[72:73], 8
	v_pk_add_f32 v[158:159], v[158:159], s[28:29] op_sel_hi:[1,0]
	v_pk_mul_f32 v[136:137], v[136:137], v[166:167]
	v_mul_f32_e32 v151, 0x4b800000, v159
	v_cmp_gt_f32_e64 s[38:39], s35, v159
	v_cmp_gt_f32_e64 s[40:41], s35, v158
	v_pk_mul_f32 v[134:135], v[134:135], v[164:165]
	v_cndmask_b32_e64 v151, v159, v151, s[38:39]
	v_rsq_f32_e32 v151, v151
	v_lshl_add_u64 v[164:165], s[12:13], 0, v[64:65]
	v_pk_fma_f32 v[108:109], v[0:1], v[108:109], 0 op_sel_hi:[1,1,0]
	v_lshlrev_b64 v[162:163], 1, v[164:165]
	v_mul_f32_e32 v159, 0x45800000, v151
	v_cndmask_b32_e64 v151, v151, v159, s[38:39]
	v_mul_f32_e32 v166, 0x3e000000, v151
	v_mul_f32_e32 v151, 0x4b800000, v158
	v_cndmask_b32_e64 v151, v158, v151, s[40:41]
	v_rsq_f32_e32 v151, v151
	v_pk_mul_f32 v[156:157], v[156:157], v[166:167] op_sel_hi:[1,0]
	v_pk_mul_f32 v[152:153], v[152:153], v[166:167] op_sel_hi:[1,0]
	v_cvt_pk_bf16_f32 v156, v156, v157
	v_cvt_pk_bf16_f32 v157, v152, v153
	v_mul_f32_e32 v152, 0x45800000, v151
	v_cndmask_b32_e64 v152, v151, v152, s[40:41]
	v_pk_fma_f32 v[108:109], v[12:13], v[84:85], v[108:109]
	v_pk_mul_f32 v[154:155], v[154:155], v[152:153] op_sel_hi:[1,0]
	v_pk_mul_f32 v[152:153], v[160:161], v[152:153] op_sel_hi:[1,0]
	v_cvt_pk_bf16_f32 v134, v134, v135
	v_cvt_pk_bf16_f32 v135, v136, v137
	v_lshl_add_u64 v[136:137], s[26:27], 0, v[162:163]
	v_pk_fma_f32 v[108:109], v[20:21], v[88:89], v[108:109]
	v_cvt_pk_bf16_f32 v154, v154, v155
	v_cvt_pk_bf16_f32 v155, v152, v153
	v_lshl_add_u64 v[152:153], s[14:15], 0, v[162:163]
	global_store_dwordx2 v[136:137], v[134:135], off
	v_pk_fma_f32 v[108:109], v[32:33], v[126:127], v[108:109]
	v_lshlrev_b32_e32 v134, 16, v146
	v_and_b32_e32 v135, 0xffff0000, v146
	global_store_dwordx2 v[152:153], v[154:155], off
	v_pk_fma_f32 v[152:153], v[48:49], v[134:135], v[108:109]
	v_pk_fma_f32 v[110:111], v[2:3], v[110:111], 0 op_sel_hi:[1,1,0]
	v_mul_f32_e32 v108, 0xbfb8aa3b, v152
	v_exp_f32_e32 v108, v108
	v_mul_f32_e32 v109, 0xbfb8aa3b, v153
	v_pk_fma_f32 v[110:111], v[14:15], v[86:87], v[110:111]
	v_exp_f32_e32 v109, v109
	v_pk_fma_f32 v[110:111], v[22:23], v[90:91], v[110:111]
	v_lshlrev_b32_e32 v136, 16, v145
	v_pk_fma_f32 v[110:111], v[34:35], v[132:133], v[110:111]
	v_and_b32_e32 v137, 0xffff0000, v145
	v_lshl_add_u64 v[164:165], s[18:19], 0, v[162:163]
	v_pk_fma_f32 v[154:155], v[50:51], v[136:137], v[110:111]
	v_add_f32_e32 v108, 1.0, v108
	global_store_dwordx2 v[164:165], v[156:157], off
	v_rcp_f32_e32 v156, v108
	v_add_f32_e32 v108, 1.0, v109
	v_mul_f32_e32 v109, 0xbfb8aa3b, v154
	v_exp_f32_e32 v109, v109
	v_mul_f32_e32 v110, 0xbfb8aa3b, v155
	v_exp_f32_e32 v110, v110
	v_rcp_f32_e32 v157, v108
	v_add_f32_e32 v108, 1.0, v109
	v_rcp_f32_e32 v158, v108
	v_add_f32_e32 v108, 1.0, v110
	v_pk_fma_f32 v[110:111], v[4:5], v[114:115], 0 op_sel_hi:[1,1,0]
	v_rcp_f32_e32 v159, v108
	v_pk_fma_f32 v[110:111], v[24:25], v[92:93], v[110:111]
	v_pk_fma_f32 v[108:109], v[6:7], v[116:117], 0 op_sel_hi:[1,1,0]
	v_pk_fma_f32 v[110:111], v[44:45], v[96:97], v[110:111]
	v_pk_fma_f32 v[108:109], v[26:27], v[94:95], v[108:109]
	v_pk_fma_f32 v[114:115], v[36:37], v[124:125], v[110:111]
	v_lshlrev_b32_e32 v110, 16, v142
	v_and_b32_e32 v111, 0xffff0000, v142
	v_pk_fma_f32 v[160:161], v[52:53], v[110:111], v[114:115]
	v_pk_fma_f32 v[108:109], v[46:47], v[98:99], v[108:109]
	v_mul_f32_e32 v114, 0xbfb8aa3b, v160
	v_exp_f32_e32 v114, v114
	v_pk_fma_f32 v[108:109], v[38:39], v[130:131], v[108:109]
	v_lshlrev_b32_e32 v116, 16, v141
	v_and_b32_e32 v117, 0xffff0000, v141
	v_mul_f32_e32 v115, 0xbfb8aa3b, v161
	v_pk_fma_f32 v[162:163], v[54:55], v[116:117], v[108:109]
	v_exp_f32_e32 v115, v115
	v_mul_f32_e32 v109, 0xbfb8aa3b, v162
	v_add_f32_e32 v108, 1.0, v114
	v_exp_f32_e32 v109, v109
	v_mul_f32_e32 v114, 0xbfb8aa3b, v163
	v_exp_f32_e32 v114, v114
	v_rcp_f32_e32 v164, v108
	v_add_f32_e32 v108, 1.0, v115
	v_rcp_f32_e32 v165, v108
	v_add_f32_e32 v108, 1.0, v109
	v_pk_fma_f32 v[86:87], v[2:3], v[86:87], 0 op_sel_hi:[1,1,0]
	v_pk_fma_f32 v[84:85], v[0:1], v[84:85], 0 op_sel_hi:[1,1,0]
	v_rcp_f32_e32 v166, v108
	v_add_f32_e32 v108, 1.0, v114
	v_pk_fma_f32 v[84:85], v[12:13], v[88:89], v[84:85]
	v_pk_fma_f32 v[86:87], v[14:15], v[90:91], v[86:87]
	v_rcp_f32_e32 v167, v108
	v_pk_fma_f32 v[108:109], v[10:11], v[120:121], 0 op_sel_hi:[1,1,0]
	v_pk_fma_f32 v[114:115], v[8:9], v[118:119], 0 op_sel_hi:[1,1,0]
	v_pk_fma_f32 v[86:87], v[22:23], v[132:133], v[86:87]
	v_pk_fma_f32 v[84:85], v[20:21], v[126:127], v[84:85]
	v_pk_fma_f32 v[114:115], v[16:17], v[100:101], v[114:115]
	v_pk_fma_f32 v[108:109], v[18:19], v[102:103], v[108:109]
	v_pk_fma_f32 v[84:85], v[32:33], v[134:135], v[84:85]
	v_pk_fma_f32 v[86:87], v[34:35], v[136:137], v[86:87]
	v_lshlrev_b32_e32 v88, 16, v150
	v_and_b32_e32 v89, 0xffff0000, v150
	v_lshlrev_b32_e32 v90, 16, v149
	v_and_b32_e32 v91, 0xffff0000, v149
	v_pk_fma_f32 v[94:95], v[6:7], v[94:95], 0 op_sel_hi:[1,1,0]
	v_pk_fma_f32 v[92:93], v[4:5], v[92:93], 0 op_sel_hi:[1,1,0]
	v_pk_fma_f32 v[108:109], v[30:31], v[106:107], v[108:109]
	v_pk_fma_f32 v[114:115], v[28:29], v[104:105], v[114:115]
	v_pk_fma_f32 v[84:85], v[48:49], v[88:89], v[84:85]
	v_pk_fma_f32 v[86:87], v[50:51], v[90:91], v[86:87]
	v_pk_fma_f32 v[92:93], v[24:25], v[96:97], v[92:93]
	v_pk_fma_f32 v[94:95], v[26:27], v[98:99], v[94:95]
	v_pk_fma_f32 v[118:119], v[40:41], v[122:123], v[114:115]
	v_pk_fma_f32 v[120:121], v[42:43], v[128:129], v[108:109]
	v_lshlrev_b32_e32 v108, 16, v140
	v_and_b32_e32 v109, 0xffff0000, v140
	v_mul_f32_e32 v88, 0xbfb8aa3b, v84
	v_mul_f32_e32 v89, 0xbfb8aa3b, v85
	v_mul_f32_e32 v90, 0xbfb8aa3b, v86
	v_mul_f32_e32 v91, 0xbfb8aa3b, v87
	v_pk_fma_f32 v[94:95], v[46:47], v[130:131], v[94:95]
	v_pk_fma_f32 v[92:93], v[44:45], v[124:125], v[92:93]
	v_pk_fma_f32 v[118:119], v[56:57], v[108:109], v[118:119]
	v_exp_f32_e32 v88, v88
	v_exp_f32_e32 v89, v89
	v_exp_f32_e32 v90, v90
	v_exp_f32_e32 v91, v91
	v_pk_fma_f32 v[92:93], v[36:37], v[110:111], v[92:93]
	v_pk_fma_f32 v[94:95], v[38:39], v[116:117], v[94:95]
	v_lshlrev_b32_e32 v96, 16, v148
	v_and_b32_e32 v97, 0xffff0000, v148
	v_lshlrev_b32_e32 v98, 16, v147
	v_and_b32_e32 v99, 0xffff0000, v147
	v_mul_f32_e32 v140, 0xbfb8aa3b, v119
	v_pk_fma_f32 v[92:93], v[52:53], v[96:97], v[92:93]
	v_pk_fma_f32 v[94:95], v[54:55], v[98:99], v[94:95]
	v_exp_f32_e32 v142, v140
	v_pk_mul_f32 v[140:141], v[154:155], v[158:159]
	v_pk_mul_f32 v[152:153], v[152:153], v[156:157]
	v_mul_f32_e32 v96, 0xbfb8aa3b, v92
	v_mul_f32_e32 v97, 0xbfb8aa3b, v93
	v_mul_f32_e32 v98, 0xbfb8aa3b, v94
	v_mul_f32_e32 v99, 0xbfb8aa3b, v95
	v_mov_b32_e32 v156, v153
	v_mov_b32_e32 v157, v141
	v_exp_f32_e32 v96, v96
	v_exp_f32_e32 v97, v97
	v_exp_f32_e32 v98, v98
	v_exp_f32_e32 v99, v99
	v_mov_b32_e32 v154, v152
	v_mov_b32_e32 v155, v140
	v_pk_mul_f32 v[156:157], v[156:157], v[156:157]
	v_add_f32_e32 v88, 1.0, v88
	v_add_f32_e32 v89, 1.0, v89
	v_add_f32_e32 v90, 1.0, v90
	v_add_f32_e32 v91, 1.0, v91
	v_pk_fma_f32 v[154:155], v[154:155], v[154:155], v[156:157]
	v_pk_mul_f32 v[156:157], v[162:163], v[166:167]
	v_pk_mul_f32 v[158:159], v[160:161], v[164:165]
	v_rcp_f32_e32 v88, v88
	v_rcp_f32_e32 v89, v89
	v_rcp_f32_e32 v90, v90
	v_rcp_f32_e32 v91, v91
	v_mov_b32_e32 v162, v159
	v_mov_b32_e32 v163, v157
	v_mov_b32_e32 v160, v158
	v_mov_b32_e32 v161, v156
	v_pk_mul_f32 v[162:163], v[162:163], v[162:163]
	v_add_f32_e32 v96, 1.0, v96
	v_add_f32_e32 v97, 1.0, v97
	v_add_f32_e32 v98, 1.0, v98
	v_add_f32_e32 v99, 1.0, v99
	v_pk_fma_f32 v[160:161], v[160:161], v[160:161], v[162:163]
	v_rcp_f32_e32 v96, v96
	v_rcp_f32_e32 v97, v97
	v_rcp_f32_e32 v98, v98
	v_rcp_f32_e32 v99, v99
	v_mov_b32_e32 v162, v160
	v_mov_b32_e32 v163, v154
	v_mov_b32_e32 v154, v161
	v_pk_mul_f32 v[86:87], v[86:87], v[90:91]
	v_pk_mul_f32 v[84:85], v[84:85], v[88:89]
	v_pk_add_f32 v[154:155], v[162:163], v[154:155]
	v_mov_b32_e32 v90, v85
	v_mov_b32_e32 v91, v87
	s_nop 1
	v_mov_b32_dpp v161, v155 quad_perm:[1,0,3,2] row_mask:0xf bank_mask:0xf
	s_nop 1
	v_mov_b32_dpp v160, v154 quad_perm:[1,0,3,2] row_mask:0xf bank_mask:0xf
	v_mov_b32_e32 v88, v84
	v_mov_b32_e32 v89, v86
	v_pk_mul_f32 v[90:91], v[90:91], v[90:91]
	v_pk_mul_f32 v[92:93], v[92:93], v[96:97]
	v_pk_fma_f32 v[88:89], v[88:89], v[88:89], v[90:91]
	v_pk_mul_f32 v[90:91], v[94:95], v[98:99]
	v_mov_b32_e32 v96, v93
	v_mov_b32_e32 v97, v91
	v_mov_b32_e32 v94, v92
	v_mov_b32_e32 v95, v90
	v_pk_mul_f32 v[96:97], v[96:97], v[96:97]
	s_waitcnt lgkmcnt(0)
	v_pk_add_f32 v[154:155], v[154:155], v[160:161]
	v_pk_fma_f32 v[94:95], v[94:95], v[94:95], v[96:97]
	v_mov_b32_e32 v97, v88
	v_mov_b32_e32 v96, v94
	v_mov_b32_e32 v88, v95
	s_nop 1
	v_mov_b32_dpp v161, v155 quad_perm:[2,3,0,1] row_mask:0xf bank_mask:0xf
	s_nop 1
	v_mov_b32_dpp v160, v154 quad_perm:[2,3,0,1] row_mask:0xf bank_mask:0xf
	v_pk_add_f32 v[88:89], v[96:97], v[88:89]
	s_nop 1
	v_mov_b32_dpp v95, v89 quad_perm:[1,0,3,2] row_mask:0xf bank_mask:0xf
	s_nop 1
	v_mov_b32_dpp v94, v88 quad_perm:[1,0,3,2] row_mask:0xf bank_mask:0xf
	v_lshlrev_b32_e32 v114, 16, v139
	v_and_b32_e32 v115, 0xffff0000, v139
	v_mul_f32_e32 v139, 0xbfb8aa3b, v118
	s_waitcnt lgkmcnt(0)
	v_pk_add_f32 v[154:155], v[154:155], v[160:161]
	v_exp_f32_e32 v139, v139
	s_nop 1
	v_mov_b32_dpp v161, v155 row_half_mirror row_mask:0xf bank_mask:0xf
	s_nop 1
	v_mov_b32_dpp v160, v154 row_half_mirror row_mask:0xf bank_mask:0xf
	s_waitcnt lgkmcnt(0)
	v_pk_add_f32 v[88:89], v[88:89], v[94:95]
	s_nop 1
	v_mov_b32_dpp v95, v89 quad_perm:[2,3,0,1] row_mask:0xf bank_mask:0xf
	s_nop 1
	v_mov_b32_dpp v94, v88 quad_perm:[2,3,0,1] row_mask:0xf bank_mask:0xf
	v_add_f32_e32 v139, 1.0, v139
	v_pk_fma_f32 v[120:121], v[58:59], v[114:115], v[120:121]
	v_rcp_f32_e32 v162, v139
	v_add_f32_e32 v139, 1.0, v142
	s_waitcnt lgkmcnt(0)
	v_pk_add_f32 v[154:155], v[154:155], v[160:161]
	v_rcp_f32_e32 v163, v139
	v_mul_f32_e32 v139, 0xbfb8aa3b, v120
	s_nop 1
	v_mov_b32_dpp v161, v155 row_mirror row_mask:0xf bank_mask:0xf
	s_nop 1
	v_mov_b32_dpp v160, v154 row_mirror row_mask:0xf bank_mask:0xf
	s_waitcnt lgkmcnt(0)
	v_pk_add_f32 v[88:89], v[88:89], v[94:95]
	v_exp_f32_e32 v139, v139
	v_mul_f32_e32 v142, 0xbfb8aa3b, v121
	s_nop 1
	v_mov_b32_dpp v95, v89 row_half_mirror row_mask:0xf bank_mask:0xf
	s_nop 1
	v_mov_b32_dpp v94, v88 row_half_mirror row_mask:0xf bank_mask:0xf
	v_exp_f32_e32 v142, v142
	v_add_f32_e32 v139, 1.0, v139
	s_waitcnt lgkmcnt(0)
	v_pk_add_f32 v[154:155], v[154:155], v[160:161]
	v_pk_fma_f32 v[102:103], v[10:11], v[102:103], 0 op_sel_hi:[1,1,0]
	v_rcp_f32_e32 v164, v139
	v_add_f32_e32 v139, 1.0, v142
	v_pk_add_f32 v[154:155], v[154:155], s[28:29] op_sel_hi:[1,0]
	v_pk_fma_f32 v[102:103], v[18:19], v[106:107], v[102:103]
	s_waitcnt lgkmcnt(0)
	v_pk_add_f32 v[88:89], v[88:89], v[94:95]
	v_rcp_f32_e32 v165, v139
	v_mul_f32_e32 v139, 0x4b800000, v155
	v_cmp_gt_f32_e64 s[38:39], s35, v155
	v_pk_fma_f32 v[102:103], v[30:31], v[128:129], v[102:103]
	s_nop 1
	v_mov_b32_dpp v95, v89 row_mirror row_mask:0xf bank_mask:0xf
	s_nop 1
	v_mov_b32_dpp v94, v88 row_mirror row_mask:0xf bank_mask:0xf
	v_cndmask_b32_e64 v139, v155, v139, s[38:39]
	v_pk_fma_f32 v[102:103], v[42:43], v[114:115], v[102:103]
	v_lshlrev_b32_e32 v106, 16, v143
	v_and_b32_e32 v107, 0xffff0000, v143
	v_rsq_f32_e32 v139, v139
	v_pk_fma_f32 v[102:103], v[58:59], v[106:107], v[102:103]
	v_pk_fma_f32 v[100:101], v[8:9], v[100:101], 0 op_sel_hi:[1,1,0]
	v_mul_f32_e32 v98, 0xbfb8aa3b, v102
	v_mul_f32_e32 v99, 0xbfb8aa3b, v103
	v_exp_f32_e32 v98, v98
	v_exp_f32_e32 v99, v99
	s_waitcnt lgkmcnt(0)
	v_pk_add_f32 v[88:89], v[88:89], v[94:95]
	v_mul_f32_e32 v142, 0x45800000, v139
	v_pk_fma_f32 v[100:101], v[16:17], v[104:105], v[100:101]
	v_pk_add_f32 v[88:89], v[88:89], s[28:29] op_sel_hi:[1,0]
	v_cndmask_b32_e64 v139, v139, v142, s[38:39]
	v_pk_fma_f32 v[100:101], v[28:29], v[122:123], v[100:101]
	v_mul_f32_e32 v94, 0x4b800000, v89
	v_cmp_gt_f32_e64 s[38:39], s35, v89
	v_pk_fma_f32 v[100:101], v[40:41], v[108:109], v[100:101]
	v_lshlrev_b32_e32 v104, 16, v144
	v_and_b32_e32 v105, 0xffff0000, v144
	v_add_f32_e32 v98, 1.0, v98
	v_add_f32_e32 v99, 1.0, v99
	v_cndmask_b32_e64 v89, v89, v94, s[38:39]
	v_pk_fma_f32 v[100:101], v[56:57], v[104:105], v[100:101]
	v_rcp_f32_e32 v98, v98
	v_rcp_f32_e32 v99, v99
	v_rsq_f32_e32 v89, v89
	v_cmp_gt_f32_e64 s[40:41], s35, v154
	v_mul_f32_e32 v142, 0x3e000000, v139
	v_mul_f32_e32 v139, 0x4b800000, v154
	v_mul_f32_e32 v104, 0xbfb8aa3b, v100
	v_mul_f32_e32 v105, 0xbfb8aa3b, v101
	v_cndmask_b32_e64 v139, v154, v139, s[40:41]
	v_exp_f32_e32 v104, v104
	v_exp_f32_e32 v105, v105
	v_rsq_f32_e32 v139, v139
	v_pk_mul_f32 v[98:99], v[102:103], v[98:99]
	v_mul_f32_e32 v102, 0x45800000, v89
	v_cndmask_b32_e64 v89, v89, v102, s[38:39]
	v_pk_mul_f32 v[152:153], v[152:153], v[142:143] op_sel_hi:[1,0]
	v_pk_mul_f32 v[140:141], v[140:141], v[142:143] op_sel_hi:[1,0]
	v_add_f32_e32 v96, 1.0, v104
	v_add_f32_e32 v97, 1.0, v105
	v_mul_f32_e32 v102, 0x3e000000, v89
	v_cvt_pk_bf16_f32 v152, v152, v153
	v_cvt_pk_bf16_f32 v153, v140, v141
	v_mul_f32_e32 v140, 0x45800000, v139
	v_rcp_f32_e32 v96, v96
	v_rcp_f32_e32 v97, v97
	v_pk_mul_f32 v[84:85], v[84:85], v[102:103] op_sel_hi:[1,0]
	s_lshl_b64 s[12:13], s[64:65], 8
	v_cndmask_b32_e64 v140, v139, v140, s[40:41]
	v_cmp_gt_f32_e64 s[40:41], s35, v88
	v_cvt_pk_bf16_f32 v84, v84, v85
	v_mul_f32_e32 v85, 0x4b800000, v88
	v_pk_mul_f32 v[118:119], v[118:119], v[162:163]
	v_lshl_add_u64 v[162:163], s[12:13], 0, v[64:65]
	v_cndmask_b32_e64 v85, v88, v85, s[40:41]
	v_lshlrev_b64 v[160:161], 1, v[162:163]
	s_lshl_b64 s[12:13], s[6:7], 8
	v_rsq_f32_e32 v88, v85
	v_lshl_add_u64 v[162:163], s[18:19], 0, v[160:161]
	v_pk_mul_f32 v[96:97], v[100:101], v[96:97]
	v_lshl_add_u64 v[100:101], s[12:13], 0, v[64:65]
	v_pk_mul_f32 v[120:121], v[120:121], v[164:165]
	global_store_dwordx2 v[162:163], v[152:153], off
	v_pk_mul_f32 v[152:153], v[158:159], v[140:141] op_sel_hi:[1,0]
	v_pk_mul_f32 v[140:141], v[156:157], v[140:141] op_sel_hi:[1,0]
	v_lshlrev_b64 v[94:95], 1, v[100:101]
	v_pk_mul_f32 v[86:87], v[86:87], v[102:103] op_sel_hi:[1,0]
	v_cvt_pk_bf16_f32 v152, v152, v153
	v_cvt_pk_bf16_f32 v153, v140, v141
	v_lshl_add_u64 v[140:141], s[14:15], 0, v[160:161]
	v_cvt_pk_bf16_f32 v118, v118, v119
	v_cvt_pk_bf16_f32 v119, v120, v121
	v_lshl_add_u64 v[120:121], s[26:27], 0, v[160:161]
	v_lshl_add_u64 v[100:101], s[18:19], 0, v[94:95]
	v_cvt_pk_bf16_f32 v85, v86, v87
	global_store_dwordx2 v[140:141], v[152:153], off
	global_store_dwordx2 v[120:121], v[118:119], off
	global_store_dwordx2 v[100:101], v[84:85], off
	v_mul_f32_e32 v84, 0x45800000, v88
	v_cndmask_b32_e64 v84, v88, v84, s[40:41]
	v_pk_mul_f32 v[86:87], v[92:93], v[84:85] op_sel_hi:[1,0]
	v_pk_mul_f32 v[84:85], v[90:91], v[84:85] op_sel_hi:[1,0]
	v_cvt_pk_bf16_f32 v86, v86, v87
	v_cvt_pk_bf16_f32 v87, v84, v85
	v_lshl_add_u64 v[84:85], s[14:15], 0, v[94:95]
	global_store_dwordx2 v[84:85], v[86:87], off
	v_cvt_pk_bf16_f32 v84, v96, v97
	v_cvt_pk_bf16_f32 v85, v98, v99
	v_lshl_add_u64 v[86:87], s[26:27], 0, v[94:95]
	global_store_dwordx2 v[86:87], v[84:85], off
	s_and_saveexec_b64 s[12:13], vcc
	s_xor_b64 s[38:39], exec, s[12:13]
	s_cbranch_execz .LBB0_345
	v_mul_f32_e32 v84, 0xbfb8aa3b, v112
	v_exp_f32_e32 v84, v84
	s_nop 0
	v_add_f32_e32 v84, 1.0, v84
	v_rcp_f32_e32 v84, v84

.LBB0_614:
	v_lshl_add_u64 v[10:11], s[94:95], 0, v[8:9]
	v_add_co_u32_e32 v12, vcc, 0x2f3d9000, v10
	s_mov_b32 s28, 0x359d9000
	s_nop 0
	v_addc_co_u32_e32 v13, vcc, 0, v11, vcc
	global_load_dwordx2 v[26:27], v[12:13], off
	v_add_co_u32_e32 v12, vcc, 0x315d9000, v10
	v_add_u32_e32 v42, 0x80, v42
	s_nop 0
	v_addc_co_u32_e32 v13, vcc, 0, v11, vcc
	v_add_co_u32_e32 v10, vcc, 0x359d9000, v10
	global_load_dwordx2 v[28:29], v[12:13], off
	s_nop 0
	v_addc_co_u32_e32 v11, vcc, 0, v11, vcc
	global_load_dwordx2 v[30:31], v[10:11], off
	v_lshl_add_u64 v[10:11], s[94:95], 0, v[6:7]
	v_add_co_u32_e32 v12, vcc, 0x2f3dd000, v10
	v_lshl_add_u64 v[6:7], v[6:7], 0, s[22:23]
	s_nop 0
	v_addc_co_u32_e32 v13, vcc, 0, v11, vcc
	global_load_dwordx2 v[34:35], v[12:13], off
	v_add_co_u32_e32 v12, vcc, 0x315dd000, v10
	v_lshl_add_u64 v[8:9], v[8:9], 0, s[22:23]
	s_nop 0
	v_addc_co_u32_e32 v13, vcc, 0, v11, vcc
	global_load_dwordx2 v[36:37], v[12:13], off
	v_add_co_u32_e32 v12, vcc, 0x359dd000, v10
	s_waitcnt vmcnt(4)
	v_lshlrev_b32_e32 v24, 16, v27
	v_addc_co_u32_e32 v13, vcc, 0, v11, vcc
	global_load_dwordx2 v[22:23], v[12:13], off
	v_add_co_u32_e32 v12, vcc, 0x2f3e1000, v10
	v_and_b32_e32 v25, 0xffff0000, v27
	s_nop 0
	v_addc_co_u32_e32 v13, vcc, 0, v11, vcc
	global_load_dwordx2 v[18:19], v[12:13], off
	v_add_co_u32_e32 v12, vcc, 0x315e1000, v10
	s_waitcnt vmcnt(5)
	v_lshlrev_b32_e32 v32, 16, v29
	v_addc_co_u32_e32 v13, vcc, 0, v11, vcc
	global_load_dwordx2 v[20:21], v[12:13], off
	v_add_co_u32_e32 v12, vcc, 0x359e1000, v10
	s_waitcnt vmcnt(4)
	v_lshlrev_b32_e32 v40, 16, v35
	v_and_b32_e32 v41, 0xffff0000, v35
	v_addc_co_u32_e32 v13, vcc, 0, v11, vcc
	global_load_dwordx2 v[16:17], v[12:13], off
	v_and_b32_e32 v33, 0xffff0000, v29
	s_waitcnt vmcnt(4)
	v_lshlrev_b32_e32 v64, 16, v37
	v_and_b32_e32 v65, 0xffff0000, v37
	v_pk_add_f32 v[40:41], v[40:41], v[64:65]
	v_lshlrev_b32_e32 v64, 16, v34
	v_and_b32_e32 v65, 0xffff0000, v34
	v_lshlrev_b32_e32 v34, 16, v36
	v_and_b32_e32 v35, 0xffff0000, v36
	v_pk_add_f32 v[34:35], v[64:65], v[34:35]
	v_mov_b32_e32 v65, v41
	v_mov_b32_e32 v64, v35
	v_mov_b32_e32 v36, v34
	v_mov_b32_e32 v37, v40
	v_pk_mul_f32 v[64:65], v[64:65], v[64:65]
	v_pk_add_f32 v[24:25], v[24:25], v[32:33]
	v_pk_fma_f32 v[64:65], v[36:37], v[36:37], v[64:65]
	v_lshlrev_b32_e32 v32, 16, v26
	v_and_b32_e32 v33, 0xffff0000, v26
	v_lshlrev_b32_e32 v26, 16, v28
	v_and_b32_e32 v27, 0xffff0000, v28
	v_pk_add_f32 v[26:27], v[32:33], v[26:27]
	v_mov_b32_e32 v33, v25
	v_mov_b32_e32 v32, v27
	v_mov_b32_e32 v28, v26
	v_mov_b32_e32 v29, v24
	v_pk_mul_f32 v[32:33], v[32:33], v[32:33]
	v_add_co_u32_e32 v12, vcc, 0x2f3e5000, v10
	v_pk_fma_f32 v[38:39], v[28:29], v[28:29], v[32:33]
	s_nop 0
	v_addc_co_u32_e32 v13, vcc, 0, v11, vcc
	v_add_co_u32_e32 v14, vcc, 0x315e5000, v10
	v_lshlrev_b32_e32 v28, 16, v30
	s_nop 0
	v_addc_co_u32_e32 v15, vcc, 0, v11, vcc
	v_and_b32_e32 v29, 0xffff0000, v30
	v_mul_f32_e32 v30, 0xbfb8aa3b, v28
	global_load_dwordx2 v[12:13], v[12:13], off
	v_exp_f32_e32 v30, v30
	global_load_dwordx2 v[14:15], v[14:15], off
	v_add_co_u32_e32 v10, vcc, 0x359e5000, v10
	v_add_f32_e32 v30, 1.0, v30
	s_nop 0
	v_addc_co_u32_e32 v11, vcc, 0, v11, vcc
	global_load_dwordx2 v[10:11], v[10:11], off
	v_rcp_f32_e32 v32, v30
	v_mul_f32_e32 v30, 0xbfb8aa3b, v29
	v_exp_f32_e32 v30, v30
	s_waitcnt vmcnt(6)
	v_lshlrev_b32_e32 v36, 16, v22
	v_and_b32_e32 v37, 0xffff0000, v22
	v_mul_f32_e32 v22, 0xbfb8aa3b, v36
	v_exp_f32_e32 v22, v22
	v_add_f32_e32 v30, 1.0, v30
	v_rcp_f32_e32 v33, v30
	v_lshlrev_b32_e32 v30, 16, v31
	v_add_f32_e32 v22, 1.0, v22
	v_rcp_f32_e32 v66, v22
	v_mul_f32_e32 v22, 0xbfb8aa3b, v37
	v_exp_f32_e32 v22, v22
	v_and_b32_e32 v31, 0xffff0000, v31
	v_pk_mul_f32 v[28:29], v[32:33], v[28:29]
	v_mul_f32_e32 v32, 0xbfb8aa3b, v30
	v_add_f32_e32 v22, 1.0, v22
	v_rcp_f32_e32 v67, v22
	v_mul_f32_e32 v33, 0xbfb8aa3b, v31
	v_exp_f32_e32 v32, v32
	v_exp_f32_e32 v33, v33
	v_pk_mul_f32 v[36:37], v[66:67], v[36:37]
	v_mov_b32_e32 v66, v64
	v_mov_b32_e32 v67, v38
	v_mov_b32_e32 v38, v65
	v_pk_add_f32 v[38:39], v[66:67], v[38:39]
	s_nop 1
	v_mov_b32_dpp v65, v39 quad_perm:[1,0,3,2] row_mask:0xf bank_mask:0xf
	s_nop 1
	v_mov_b32_dpp v64, v38 quad_perm:[1,0,3,2] row_mask:0xf bank_mask:0xf
	v_add_f32_e32 v32, 1.0, v32
	v_add_f32_e32 v33, 1.0, v33
	v_rcp_f32_e32 v32, v32
	v_rcp_f32_e32 v33, v33
	s_waitcnt lgkmcnt(0)
	v_pk_add_f32 v[38:39], v[38:39], v[64:65]
	s_nop 1
	v_mov_b32_dpp v65, v39 quad_perm:[2,3,0,1] row_mask:0xf bank_mask:0xf
	s_nop 1
	v_mov_b32_dpp v64, v38 quad_perm:[2,3,0,1] row_mask:0xf bank_mask:0xf
	v_pk_mul_f32 v[30:31], v[32:33], v[30:31]
	v_lshl_add_u64 v[32:33], s[94:95], 0, v[4:5]
	v_lshl_add_u64 v[4:5], v[4:5], 0, s[22:23]
	s_waitcnt lgkmcnt(0)
	v_pk_add_f32 v[38:39], v[38:39], v[64:65]
	s_nop 1
	v_mov_b32_dpp v65, v39 row_half_mirror row_mask:0xf bank_mask:0xf
	s_nop 1
	v_mov_b32_dpp v64, v38 row_half_mirror row_mask:0xf bank_mask:0xf
	s_waitcnt lgkmcnt(0)
	v_pk_add_f32 v[38:39], v[38:39], v[64:65]
	s_nop 1
	v_mov_b32_dpp v65, v39 row_mirror row_mask:0xf bank_mask:0xf
	s_nop 1
	v_mov_b32_dpp v64, v38 row_mirror row_mask:0xf bank_mask:0xf
	s_waitcnt lgkmcnt(0)
	v_pk_add_f32 v[38:39], v[38:39], v[64:65]
	v_mov_b64_e32 v[64:65], s[30:31]
	v_pk_fma_f32 v[38:39], v[38:39], s[36:37], v[64:65] op_sel_hi:[1,0,0]
	s_nop 0
	v_mul_f32_e32 v22, 0x4b800000, v39
	v_cmp_gt_f32_e64 s[42:43], s35, v39
	v_cmp_gt_f32_e32 vcc, s35, v38
	s_nop 0
	v_cndmask_b32_e64 v22, v39, v22, s[42:43]
	v_rsq_f32_e32 v22, v22
	s_nop 0
	v_mul_f32_e32 v39, 0x45800000, v22
	v_cndmask_b32_e64 v22, v22, v39, s[42:43]
	v_pk_mul_f32 v[26:27], v[26:27], v[22:23] op_sel_hi:[1,0]
	v_pk_mul_f32 v[24:25], v[24:25], v[22:23] op_sel_hi:[1,0]
	v_mul_f32_e32 v22, 0x4b800000, v38
	v_cndmask_b32_e32 v22, v38, v22, vcc
	v_pk_mul_f32 v[26:27], v[0:1], v[26:27]
	v_pk_mul_f32 v[24:25], v[2:3], v[24:25]
	v_rsq_f32_e32 v22, v22
	v_pk_mul_f32 v[26:27], v[28:29], v[26:27]
	v_pk_mul_f32 v[24:25], v[30:31], v[24:25]
	v_cvt_pk_bf16_f32 v26, v26, v27
	v_cvt_pk_bf16_f32 v27, v24, v25
	v_add_co_u32_e64 v24, s[42:43], s28, v32
	s_mov_b32 s28, 0x359dd000
	s_nop 0
	v_addc_co_u32_e64 v25, s[42:43], 0, v33, s[42:43]
	global_store_dwordx2 v[24:25], v[26:27], off
	v_mul_f32_e32 v24, 0x45800000, v22
	v_cndmask_b32_e32 v22, v22, v24, vcc
	v_pk_mul_f32 v[24:25], v[34:35], v[22:23] op_sel_hi:[1,0]
	v_lshlrev_b32_e32 v26, 16, v23
	v_pk_mul_f32 v[24:25], v[0:1], v[24:25]
	v_and_b32_e32 v27, 0xffff0000, v23
	v_pk_mul_f32 v[24:25], v[36:37], v[24:25]
	v_mul_f32_e32 v23, 0xbfb8aa3b, v26
	v_cvt_pk_bf16_f32 v24, v24, v25
	v_mul_f32_e32 v25, 0xbfb8aa3b, v27
	v_exp_f32_e32 v23, v23
	v_exp_f32_e32 v25, v25
	v_add_f32_e32 v23, 1.0, v23
	v_add_f32_e32 v25, 1.0, v25
	v_rcp_f32_e32 v28, v23
	v_rcp_f32_e32 v29, v25
	v_pk_mul_f32 v[22:23], v[40:41], v[22:23] op_sel_hi:[1,0]
	v_pk_mul_f32 v[26:27], v[28:29], v[26:27]
	v_pk_mul_f32 v[22:23], v[2:3], v[22:23]
	s_waitcnt vmcnt(2)
	v_lshlrev_b32_e32 v28, 16, v15
	v_pk_mul_f32 v[22:23], v[26:27], v[22:23]
	v_and_b32_e32 v29, 0xffff0000, v15
	v_cvt_pk_bf16_f32 v25, v22, v23
	v_add_co_u32_e32 v22, vcc, s28, v32
	s_mov_b32 s28, 0x359e1000
	s_nop 0
	v_addc_co_u32_e32 v23, vcc, 0, v33, vcc
	global_store_dwordx2 v[22:23], v[24:25], off
	v_lshlrev_b32_e32 v22, 16, v19
	v_and_b32_e32 v23, 0xffff0000, v19
	v_lshlrev_b32_e32 v24, 16, v21
	v_and_b32_e32 v25, 0xffff0000, v21
	v_pk_add_f32 v[22:23], v[22:23], v[24:25]
	v_lshlrev_b32_e32 v24, 16, v18
	v_and_b32_e32 v25, 0xffff0000, v18
	v_lshlrev_b32_e32 v18, 16, v20
	v_and_b32_e32 v19, 0xffff0000, v20
	v_pk_add_f32 v[18:19], v[24:25], v[18:19]
	v_mov_b32_e32 v25, v23
	v_mov_b32_e32 v24, v19
	v_mov_b32_e32 v20, v18
	v_mov_b32_e32 v21, v22
	v_pk_mul_f32 v[24:25], v[24:25], v[24:25]
	s_nop 0
	v_pk_fma_f32 v[20:21], v[20:21], v[20:21], v[24:25]
	v_lshlrev_b32_e32 v24, 16, v16
	v_and_b32_e32 v25, 0xffff0000, v16
	v_mul_f32_e32 v16, 0xbfb8aa3b, v24
	v_exp_f32_e32 v16, v16
	s_nop 0
	v_add_f32_e32 v16, 1.0, v16
	v_rcp_f32_e32 v26, v16
	v_mul_f32_e32 v16, 0xbfb8aa3b, v25
	v_exp_f32_e32 v16, v16
	s_nop 0
	v_add_f32_e32 v16, 1.0, v16
	v_rcp_f32_e32 v27, v16
	v_lshlrev_b32_e32 v16, 16, v17
	v_and_b32_e32 v17, 0xffff0000, v17
	v_pk_mul_f32 v[24:25], v[26:27], v[24:25]
	v_mul_f32_e32 v26, 0xbfb8aa3b, v16
	v_mul_f32_e32 v27, 0xbfb8aa3b, v17
	v_exp_f32_e32 v26, v26
	v_exp_f32_e32 v27, v27
	v_add_f32_e32 v26, 1.0, v26
	v_add_f32_e32 v27, 1.0, v27
	v_rcp_f32_e32 v26, v26
	v_rcp_f32_e32 v27, v27
	s_nop 0
	v_pk_mul_f32 v[16:17], v[26:27], v[16:17]
	v_lshlrev_b32_e32 v26, 16, v13
	v_and_b32_e32 v27, 0xffff0000, v13
	v_pk_add_f32 v[26:27], v[26:27], v[28:29]
	v_lshlrev_b32_e32 v28, 16, v12
	v_and_b32_e32 v29, 0xffff0000, v12
	v_lshlrev_b32_e32 v12, 16, v14
	v_and_b32_e32 v13, 0xffff0000, v14
	v_pk_add_f32 v[12:13], v[28:29], v[12:13]
	v_mov_b32_e32 v29, v27
	v_mov_b32_e32 v28, v13
	v_mov_b32_e32 v14, v12
	v_mov_b32_e32 v15, v26
	v_pk_mul_f32 v[28:29], v[28:29], v[28:29]
	s_nop 0
	v_pk_fma_f32 v[14:15], v[14:15], v[14:15], v[28:29]
	s_waitcnt vmcnt(2)
	v_lshlrev_b32_e32 v28, 16, v10
	v_and_b32_e32 v29, 0xffff0000, v10
	v_mul_f32_e32 v10, 0xbfb8aa3b, v28
	v_exp_f32_e32 v10, v10
	s_nop 0
	v_add_f32_e32 v10, 1.0, v10
	v_rcp_f32_e32 v30, v10
	v_mul_f32_e32 v10, 0xbfb8aa3b, v29
	v_exp_f32_e32 v10, v10
	s_nop 0
	v_add_f32_e32 v10, 1.0, v10
	v_rcp_f32_e32 v31, v10
	s_nop 0
	v_pk_mul_f32 v[28:29], v[30:31], v[28:29]
	v_mov_b32_e32 v30, v14
	v_mov_b32_e32 v31, v20
	v_mov_b32_e32 v20, v15
	v_pk_add_f32 v[14:15], v[30:31], v[20:21]
	s_nop 1
	v_mov_b32_dpp v21, v15 quad_perm:[1,0,3,2] row_mask:0xf bank_mask:0xf
	s_nop 1
	v_mov_b32_dpp v20, v14 quad_perm:[1,0,3,2] row_mask:0xf bank_mask:0xf
	s_waitcnt lgkmcnt(0)
	v_pk_add_f32 v[14:15], v[14:15], v[20:21]
	s_nop 1
	v_mov_b32_dpp v21, v15 quad_perm:[2,3,0,1] row_mask:0xf bank_mask:0xf
	s_nop 1
	v_mov_b32_dpp v20, v14 quad_perm:[2,3,0,1] row_mask:0xf bank_mask:0xf
	s_waitcnt lgkmcnt(0)
	v_pk_add_f32 v[14:15], v[14:15], v[20:21]
	s_nop 1
	v_mov_b32_dpp v21, v15 row_half_mirror row_mask:0xf bank_mask:0xf
	s_nop 1
	v_mov_b32_dpp v20, v14 row_half_mirror row_mask:0xf bank_mask:0xf
	s_waitcnt lgkmcnt(0)
	v_pk_add_f32 v[14:15], v[14:15], v[20:21]
	s_nop 1
	v_mov_b32_dpp v21, v15 row_mirror row_mask:0xf bank_mask:0xf
	s_nop 1
	v_mov_b32_dpp v20, v14 row_mirror row_mask:0xf bank_mask:0xf
	s_waitcnt lgkmcnt(0)
	v_pk_add_f32 v[14:15], v[14:15], v[20:21]
	s_nop 0
	v_pk_fma_f32 v[14:15], v[14:15], s[36:37], v[64:65] op_sel_hi:[1,0,0]
	s_nop 0
	v_mul_f32_e32 v10, 0x4b800000, v15
	v_cmp_gt_f32_e64 s[42:43], s35, v15
	v_cmp_gt_f32_e32 vcc, s35, v14
	s_nop 0
	v_cndmask_b32_e64 v10, v15, v10, s[42:43]
	v_rsq_f32_e32 v10, v10
	s_nop 0
	v_mul_f32_e32 v15, 0x45800000, v10
	v_cndmask_b32_e64 v10, v10, v15, s[42:43]
	v_pk_mul_f32 v[18:19], v[18:19], v[10:11] op_sel_hi:[1,0]
	v_pk_mul_f32 v[20:21], v[22:23], v[10:11] op_sel_hi:[1,0]
	v_mul_f32_e32 v10, 0x4b800000, v14
	v_cndmask_b32_e32 v10, v14, v10, vcc
	v_rsq_f32_e32 v10, v10
	v_and_b32_e32 v15, 0xffff0000, v11
	v_pk_mul_f32 v[18:19], v[0:1], v[18:19]
	v_pk_mul_f32 v[20:21], v[2:3], v[20:21]
	v_mul_f32_e32 v14, 0x45800000, v10
	v_cndmask_b32_e32 v10, v10, v14, vcc
	v_pk_mul_f32 v[12:13], v[12:13], v[10:11] op_sel_hi:[1,0]
	v_lshlrev_b32_e32 v14, 16, v11
	v_pk_mul_f32 v[12:13], v[0:1], v[12:13]
	v_mul_f32_e32 v11, 0xbfb8aa3b, v14
	v_pk_mul_f32 v[12:13], v[28:29], v[12:13]
	v_exp_f32_e32 v11, v11
	v_cvt_pk_bf16_f32 v12, v12, v13
	v_mul_f32_e32 v13, 0xbfb8aa3b, v15
	v_exp_f32_e32 v13, v13
	v_pk_mul_f32 v[18:19], v[24:25], v[18:19]
	v_pk_mul_f32 v[16:17], v[16:17], v[20:21]
	v_cvt_pk_bf16_f32 v18, v18, v19
	v_cvt_pk_bf16_f32 v19, v16, v17
	v_add_co_u32_e64 v16, s[42:43], s28, v32
	v_add_f32_e32 v11, 1.0, v11
	s_nop 0
	v_addc_co_u32_e64 v17, s[42:43], 0, v33, s[42:43]
	v_add_f32_e32 v13, 1.0, v13
	global_store_dwordx2 v[16:17], v[18:19], off
	v_rcp_f32_e32 v16, v11
	v_rcp_f32_e32 v17, v13
	v_pk_mul_f32 v[10:11], v[26:27], v[10:11] op_sel_hi:[1,0]
	s_movk_i32 s28, 0x107f
	v_pk_mul_f32 v[10:11], v[2:3], v[10:11]
	v_pk_mul_f32 v[14:15], v[16:17], v[14:15]
	s_nop 0
	v_pk_mul_f32 v[10:11], v[14:15], v[10:11]
	s_nop 0
	v_cvt_pk_bf16_f32 v13, v10, v11
	v_add_co_u32_e32 v10, vcc, 0x359e5000, v32
	s_nop 1
	v_addc_co_u32_e32 v11, vcc, 0, v33, vcc
	v_cmp_lt_i32_e32 vcc, s28, v42
	s_or_b64 s[46:47], vcc, s[46:47]
	global_store_dwordx2 v[10:11], v[12:13], off
	s_andn2_b64 exec, exec, s[46:47]
	s_cbranch_execnz .LBB0_614
	s_branch .LBB0_605

.LBB0_922:
	s_add_i32 s26, s4, s2
	s_ashr_i32 s6, s26, 12
	s_mulk_i32 s6, 0x1100
	s_add_i32 s27, s6, 0x100
	s_and_b32 s6, s26, 0xffc
	v_readlane_b32 vcc_lo, v252, 6
	s_add_i32 s28, s27, s6
	v_readlane_b32 vcc_hi, v252, 7
	s_and_b64 s[6:7], vcc, exec
	s_cselect_b32 s70, s26, s28
	s_mul_hi_i32 s6, s70, 0x78787879
	s_lshr_b32 s7, s6, 31
	s_ashr_i32 s6, s6, 11
	s_add_i32 s6, s6, s7
	s_mul_i32 s7, s6, 0xffffef00
	s_add_i32 s7, s7, s70
	s_cmpk_gt_i32 s7, 0xff
	s_cselect_b32 s33, s6, 16
	s_ashr_i32 s71, s70, 31
	s_lshl_b64 s[64:65], s[70:71], 11
	v_lshl_add_u64 v[32:33], v[58:59], 0, s[64:65]
	global_load_dwordx4 v[70:73], v[32:33], off
	global_load_dwordx4 v[74:77], v[32:33], off offset:1024
	s_add_i32 s28, s26, 1
	s_and_b32 s6, s28, 0xffd
	s_add_i32 s29, s27, s6
	s_and_b64 s[6:7], vcc, exec
	s_cselect_b32 s48, s28, s29
	s_add_i32 s28, s26, 2
	s_ashr_i32 s49, s48, 31
	s_and_b32 s6, s28, 0xffe
	s_lshl_b64 s[46:47], s[48:49], 11
	s_add_i32 s29, s27, s6
	s_and_b64 s[6:7], vcc, exec
	s_cselect_b32 s42, s28, s29
	s_add_i32 s26, s26, 3
	s_ashr_i32 s43, s42, 31
	s_and_b32 s6, s26, 0xfff
	s_lshl_b64 s[40:41], s[42:43], 11
	s_add_i32 s27, s27, s6
	s_and_b64 s[6:7], vcc, exec
	s_cselect_b32 s26, s26, s27
	v_lshl_add_u64 v[32:33], v[58:59], 0, s[46:47]
	s_ashr_i32 s27, s26, 31
	global_load_dwordx4 v[52:55], v[32:33], off
	global_load_dwordx4 v[48:51], v[32:33], off offset:1024
	v_lshl_add_u64 v[32:33], v[58:59], 0, s[40:41]
	s_lshl_b64 s[6:7], s[26:27], 11
	global_load_dwordx4 v[44:47], v[32:33], off
	global_load_dwordx4 v[40:43], v[32:33], off offset:1024
	v_lshl_add_u64 v[32:33], v[58:59], 0, s[6:7]
	global_load_dwordx4 v[36:39], v[32:33], off
	s_nop 0
	global_load_dwordx4 v[32:35], v[32:33], off offset:1024
	s_cmp_eq_u32 s33, s14
	s_waitcnt vmcnt(7)
	v_and_b32_e32 v97, 0xffff0000, v70
	v_and_b32_e32 v93, 0xffff0000, v71
	v_lshlrev_b32_e32 v96, 16, v70
	v_lshlrev_b32_e32 v92, 16, v71
	v_mul_f32_e32 v70, v97, v97
	v_mul_f32_e32 v71, v93, v93
	v_and_b32_e32 v89, 0xffff0000, v72
	v_and_b32_e32 v87, 0xffff0000, v73
	v_fmac_f32_e32 v70, v96, v96
	v_fmac_f32_e32 v71, v92, v92
	v_lshlrev_b32_e32 v88, 16, v72
	v_lshlrev_b32_e32 v86, 16, v73
	v_add_f32_e32 v70, v70, v71
	v_mul_f32_e32 v71, v89, v89
	v_mul_f32_e32 v72, v87, v87
	v_fmac_f32_e32 v71, v88, v88
	v_fmac_f32_e32 v72, v86, v86
	v_add_f32_e32 v71, v71, v72
	s_waitcnt vmcnt(6)
	v_and_b32_e32 v83, 0xffff0000, v74
	v_and_b32_e32 v85, 0xffff0000, v75
	v_add_f32_e32 v70, v70, v71
	v_lshlrev_b32_e32 v82, 16, v74
	v_lshlrev_b32_e32 v84, 16, v75
	v_mul_f32_e32 v71, v83, v83
	v_mul_f32_e32 v72, v85, v85
	v_and_b32_e32 v79, 0xffff0000, v76
	v_and_b32_e32 v81, 0xffff0000, v77
	v_fmac_f32_e32 v71, v82, v82
	v_fmac_f32_e32 v72, v84, v84
	v_lshlrev_b32_e32 v78, 16, v76
	v_lshlrev_b32_e32 v80, 16, v77
	v_add_f32_e32 v71, v71, v72
	v_mul_f32_e32 v72, v79, v79
	v_mul_f32_e32 v73, v81, v81
	v_fmac_f32_e32 v72, v78, v78
	v_fmac_f32_e32 v73, v80, v80
	v_add_f32_e32 v72, v72, v73
	v_add_f32_e32 v71, v71, v72
	v_add_f32_e32 v70, v70, v71
	s_nop 1
	v_mov_b32_dpp v71, v70 quad_perm:[1,0,3,2] row_mask:0xf bank_mask:0xf
	s_waitcnt lgkmcnt(0)
	v_add_f32_e32 v70, v70, v71
	s_nop 1
	v_mov_b32_dpp v71, v70 quad_perm:[2,3,0,1] row_mask:0xf bank_mask:0xf
	s_waitcnt lgkmcnt(0)
	v_add_f32_e32 v70, v70, v71
	s_nop 1
	v_mov_b32_dpp v71, v70 row_half_mirror row_mask:0xf bank_mask:0xf
	s_waitcnt lgkmcnt(0)
	v_add_f32_e32 v70, v70, v71
	s_nop 1
	v_mov_b32_dpp v71, v70 row_mirror row_mask:0xf bank_mask:0xf
	s_waitcnt lgkmcnt(0)
	v_add_f32_e32 v70, v70, v71
	ds_swizzle_b32 v71, v70 offset:swizzle(SWAP,16)
	s_waitcnt lgkmcnt(0)
	v_add_f32_e32 v104, v70, v71
	v_mov_b32_e32 v105, v104
	s_nop 1
	v_permlane32_swap_b32_e32 v104, v105
	s_cbranch_scc1 .LBB0_924
	s_add_i32 s14, s33, s13
	s_mul_hi_i32 s29, s14, 0x6000
	s_mulk_i32 s14, 0x6000
	s_add_u32 s28, s60, s14
	s_addc_u32 s29, s63, s29
	v_lshl_add_u64 v[16:17], v[56:57], 2, s[28:29]
	v_add_co_u32_e32 v8, vcc, 0x4000, v16
	s_mov_b64 s[28:29], 0x4000
	s_nop 0
	v_addc_co_u32_e32 v9, vcc, 0, v17, vcc
	global_load_dwordx4 v[4:7], v[60:61], off offset:16
	global_load_dwordx4 v[0:3], v[60:61], off
	v_lshl_add_u64 v[28:29], v[16:17], 0, s[28:29]
	global_load_dwordx4 v[8:11], v[8:9], off
	s_nop 0
	global_load_dwordx4 v[12:15], v[28:29], off offset:16
	s_movk_i32 s14, 0x3000
	s_mov_b64 s[28:29], 0x3000
	v_lshl_add_u64 v[70:71], v[16:17], 0, s[28:29]
	s_waitcnt vmcnt(1)
	v_pk_add_f32 v[8:9], v[8:9], 1.0 op_sel_hi:[1,0]
	s_nop 0
	v_pk_mul_f32 v[0:1], v[0:1], v[8:9]
	s_waitcnt vmcnt(0)
	v_pk_add_f32 v[8:9], v[14:15], 1.0 op_sel_hi:[1,0]
	v_pk_add_f32 v[10:11], v[10:11], 1.0 op_sel_hi:[1,0]
	v_pk_mul_f32 v[6:7], v[6:7], v[8:9]
	v_add_co_u32_e32 v8, vcc, s14, v16
	v_pk_mul_f32 v[2:3], v[2:3], v[10:11]
	v_pk_add_f32 v[10:11], v[12:13], 1.0 op_sel_hi:[1,0]
	v_addc_co_u32_e32 v9, vcc, 0, v17, vcc
	v_pk_mul_f32 v[4:5], v[4:5], v[10:11]
	global_load_dwordx4 v[8:11], v[8:9], off
	s_nop 0
	global_load_dwordx4 v[12:15], v[70:71], off offset:16
	global_load_dwordx4 v[20:23], v[60:61], off offset:2064
	global_load_dwordx4 v[16:19], v[60:61], off offset:2048
	global_load_dwordx4 v[24:27], v[28:29], off offset:2064
	s_nop 0
	global_load_dwordx4 v[28:31], v[28:29], off offset:2048
	s_mov_b32 s14, s33
	s_waitcnt vmcnt(1)
	v_pk_add_f32 v[26:27], v[26:27], 1.0 op_sel_hi:[1,0]
	s_waitcnt vmcnt(0)
	v_pk_add_f32 v[30:31], v[30:31], 1.0 op_sel_hi:[1,0]
	v_pk_add_f32 v[28:29], v[28:29], 1.0 op_sel_hi:[1,0]
	v_pk_add_f32 v[24:25], v[24:25], 1.0 op_sel_hi:[1,0]
	v_pk_mul_f32 v[18:19], v[18:19], v[30:31]
	v_pk_mul_f32 v[16:17], v[16:17], v[28:29]
	v_pk_mul_f32 v[22:23], v[22:23], v[26:27]
	v_pk_mul_f32 v[20:21], v[20:21], v[24:25]
	global_load_dwordx4 v[24:27], v[70:71], off offset:2064
	global_load_dwordx4 v[28:31], v[70:71], off offset:2048
.LBB0_924:
	s_waitcnt vmcnt(5)
	v_and_b32_e32 v101, 0xffff0000, v52
	v_and_b32_e32 v99, 0xffff0000, v53
	v_lshlrev_b32_e32 v100, 16, v52
	v_lshlrev_b32_e32 v98, 16, v53
	v_mul_f32_e32 v52, v101, v101
	v_mul_f32_e32 v53, v99, v99
	v_and_b32_e32 v95, 0xffff0000, v54
	v_and_b32_e32 v91, 0xffff0000, v55
	v_fmac_f32_e32 v52, v100, v100
	v_fmac_f32_e32 v53, v98, v98
	v_lshlrev_b32_e32 v94, 16, v54
	v_lshlrev_b32_e32 v90, 16, v55
	v_add_f32_e32 v52, v52, v53
	v_mul_f32_e32 v53, v95, v95
	v_mul_f32_e32 v54, v91, v91
	v_fmac_f32_e32 v53, v94, v94
	v_fmac_f32_e32 v54, v90, v90
	s_waitcnt vmcnt(4)
	v_lshlrev_b32_e32 v74, 16, v51
	v_and_b32_e32 v75, 0xffff0000, v51
	v_add_f32_e32 v51, v104, v105
	v_add_f32_e32 v53, v53, v54
	v_and_b32_e32 v73, 0xffff0000, v48
	v_and_b32_e32 v77, 0xffff0000, v49
	v_fmamk_f32 v51, v51, 0x3a800000, v196
	v_add_f32_e32 v52, v52, v53
	v_lshlrev_b32_e32 v72, 16, v48
	v_lshlrev_b32_e32 v76, 16, v49
	v_mul_f32_e32 v48, v73, v73
	v_mul_f32_e32 v49, v77, v77
	v_mul_f32_e32 v53, 0x4b800000, v51
	v_cmp_gt_f32_e32 vcc, s35, v51
	v_and_b32_e32 v71, 0xffff0000, v50
	v_fmac_f32_e32 v48, v72, v72
	v_fmac_f32_e32 v49, v76, v76
	v_cndmask_b32_e32 v51, v51, v53, vcc
	v_lshlrev_b32_e32 v70, 16, v50
	v_add_f32_e32 v48, v48, v49
	v_mul_f32_e32 v49, v71, v71
	v_mul_f32_e32 v50, v75, v75
	v_rsq_f32_e32 v51, v51
	v_fmac_f32_e32 v49, v70, v70
	v_fmac_f32_e32 v50, v74, v74
	v_add_f32_e32 v49, v49, v50
	v_add_f32_e32 v48, v48, v49
	v_add_f32_e32 v53, v52, v48
	v_mul_f32_e32 v48, 0x45800000, v51
	v_cndmask_b32_e32 v52, v51, v48, vcc
	v_pk_mul_f32 v[48:49], v[52:53], v[96:97] op_sel_hi:[0,1]
	v_pk_mul_f32 v[50:51], v[52:53], v[92:93] op_sel_hi:[0,1]
	v_pk_fma_f32 v[54:55], v[50:51], v[2:3], v[10:11]
	v_pk_fma_f32 v[50:51], v[48:49], v[0:1], v[8:9]
	v_pk_mul_f32 v[48:49], v[52:53], v[88:89] op_sel_hi:[0,1]
	v_pk_fma_f32 v[88:89], v[48:49], v[4:5], v[12:13]
	v_mov_b32_e32 v92, v113
	v_mov_b32_e32 v93, v113
	v_cvt_pk_bf16_f32 v48, v50, v51
	v_cvt_pk_fp8_f32 v92, v50, v51
	v_cvt_pk_fp8_f32 v93, v88, v89
	v_cvt_pk_bf16_f32 v50, v88, v89
	s_nop 1
	v_mov_b32_dpp v88, v53 quad_perm:[1,0,3,2] row_mask:0xf bank_mask:0xf
	v_pk_mul_f32 v[86:87], v[52:53], v[86:87] op_sel_hi:[0,1]
	v_pk_fma_f32 v[86:87], v[86:87], v[6:7], v[14:15]
	v_cvt_pk_bf16_f32 v49, v54, v55
	v_cvt_pk_bf16_f32 v51, v86, v87
	v_cvt_pk_fp8_f32 v92, v54, v55 op_sel:[0,0,1]
	v_lshl_add_u64 v[54:55], v[62:63], 0, s[64:65]
	global_store_dwordx4 v[54:55], v[48:51], off
	v_pk_mul_f32 v[78:79], v[52:53], v[78:79] op_sel_hi:[0,1]
	s_mul_hi_i32 s28, s48, 0x78787879
	v_pk_mul_f32 v[48:49], v[52:53], v[82:83] op_sel_hi:[0,1]
	s_waitcnt lgkmcnt(0)
	v_add_f32_e32 v82, v53, v88
	s_nop 1
	v_mov_b32_dpp v83, v82 quad_perm:[2,3,0,1] row_mask:0xf bank_mask:0xf
	v_pk_mul_f32 v[50:51], v[52:53], v[84:85] op_sel_hi:[0,1]
	s_waitcnt vmcnt(1)
	v_pk_fma_f32 v[48:49], v[48:49], v[16:17], v[28:29]
	v_pk_mul_f32 v[52:53], v[52:53], v[80:81] op_sel_hi:[0,1]
	v_pk_fma_f32 v[78:79], v[78:79], v[20:21], v[24:25]
	s_waitcnt lgkmcnt(0)
	v_add_f32_e32 v82, v82, v83
	s_nop 1
	v_mov_b32_dpp v83, v82 row_half_mirror row_mask:0xf bank_mask:0xf
	v_mov_b32_e32 v80, v113
	v_mov_b32_e32 v81, v113
	s_lshr_b32 s29, s28, 31
	s_ashr_i32 s28, s28, 11
	s_waitcnt lgkmcnt(0)
	v_add_f32_e32 v82, v82, v83
	s_nop 1
	v_mov_b32_dpp v83, v82 row_mirror row_mask:0xf bank_mask:0xf
	v_cvt_pk_fp8_f32 v80, v48, v49
	v_cvt_pk_fp8_f32 v81, v78, v79
	s_add_i32 s28, s28, s29
	s_mul_i32 s29, s28, 0xffffef00
	s_waitcnt lgkmcnt(0)
	v_add_f32_e32 v82, v82, v83
	ds_swizzle_b32 v83, v82 offset:swizzle(SWAP,16)
	s_add_i32 s29, s29, s48
	v_cvt_pk_fp8_f32 v93, v86, v87 op_sel:[0,0,1]
	v_pk_fma_f32 v[50:51], v[50:51], v[18:19], v[30:31]
	v_pk_fma_f32 v[52:53], v[52:53], v[22:23], v[26:27]
	s_cmpk_gt_i32 s29, 0xff
	v_cvt_pk_fp8_f32 v80, v50, v51 op_sel:[0,0,1]
	v_cvt_pk_fp8_f32 v81, v52, v53 op_sel:[0,0,1]
	s_cselect_b32 s33, s28, 16
	s_lshl_b64 s[28:29], s[70:71], 10
	v_lshl_add_u64 v[86:87], v[68:69], 0, s[28:29]
	v_cvt_pk_bf16_f32 v48, v48, v49
	v_cvt_pk_bf16_f32 v49, v50, v51
	v_cvt_pk_bf16_f32 v50, v78, v79
	v_cvt_pk_bf16_f32 v51, v52, v53
	global_store_dwordx2 v[86:87], v[92:93], off
	global_store_dwordx4 v[54:55], v[48:51], off offset:1024
	global_store_dwordx2 v[86:87], v[80:81], off offset:512
	s_cmp_eq_u32 s33, s14
	s_waitcnt lgkmcnt(0)
	v_add_f32_e32 v48, v82, v83
	v_mov_b32_e32 v49, v48
	s_nop 1
	v_permlane32_swap_b32_e32 v48, v49
	s_cbranch_scc1 .LBB0_926
	s_add_i32 s14, s33, s13
	s_mul_hi_i32 s29, s14, 0x6000
	s_mulk_i32 s14, 0x6000
	s_add_u32 s28, s60, s14
	s_addc_u32 s29, s63, s29
	v_lshl_add_u64 v[16:17], v[56:57], 2, s[28:29]
	v_add_co_u32_e32 v8, vcc, 0x4000, v16
	s_mov_b64 s[28:29], 0x4000
	s_nop 0
	v_addc_co_u32_e32 v9, vcc, 0, v17, vcc
	global_load_dwordx4 v[4:7], v[60:61], off offset:16
	global_load_dwordx4 v[0:3], v[60:61], off
	v_lshl_add_u64 v[28:29], v[16:17], 0, s[28:29]
	global_load_dwordx4 v[8:11], v[8:9], off
	s_nop 0
	global_load_dwordx4 v[12:15], v[28:29], off offset:16
	s_movk_i32 s14, 0x3000
	s_mov_b64 s[28:29], 0x3000
	v_lshl_add_u64 v[50:51], v[16:17], 0, s[28:29]
	s_waitcnt vmcnt(1)
	v_pk_add_f32 v[8:9], v[8:9], 1.0 op_sel_hi:[1,0]
	s_nop 0
	v_pk_mul_f32 v[0:1], v[0:1], v[8:9]
	s_waitcnt vmcnt(0)
	v_pk_add_f32 v[8:9], v[14:15], 1.0 op_sel_hi:[1,0]
	v_pk_add_f32 v[10:11], v[10:11], 1.0 op_sel_hi:[1,0]
	v_pk_mul_f32 v[6:7], v[6:7], v[8:9]
	v_add_co_u32_e32 v8, vcc, s14, v16
	v_pk_mul_f32 v[2:3], v[2:3], v[10:11]
	v_pk_add_f32 v[10:11], v[12:13], 1.0 op_sel_hi:[1,0]
	v_addc_co_u32_e32 v9, vcc, 0, v17, vcc
	v_pk_mul_f32 v[4:5], v[4:5], v[10:11]
	global_load_dwordx4 v[8:11], v[8:9], off
	s_nop 0
	global_load_dwordx4 v[12:15], v[50:51], off offset:16
	global_load_dwordx4 v[20:23], v[60:61], off offset:2064
	global_load_dwordx4 v[16:19], v[60:61], off offset:2048
	global_load_dwordx4 v[24:27], v[28:29], off offset:2064
	s_nop 0
	global_load_dwordx4 v[28:31], v[28:29], off offset:2048
	s_waitcnt vmcnt(1)
	v_pk_add_f32 v[26:27], v[26:27], 1.0 op_sel_hi:[1,0]
	s_waitcnt vmcnt(0)
	v_pk_add_f32 v[30:31], v[30:31], 1.0 op_sel_hi:[1,0]
	v_pk_add_f32 v[28:29], v[28:29], 1.0 op_sel_hi:[1,0]
	v_pk_add_f32 v[24:25], v[24:25], 1.0 op_sel_hi:[1,0]
	v_pk_mul_f32 v[18:19], v[18:19], v[30:31]
	v_pk_mul_f32 v[16:17], v[16:17], v[28:29]
	v_pk_mul_f32 v[22:23], v[22:23], v[26:27]
	v_pk_mul_f32 v[20:21], v[20:21], v[24:25]
	global_load_dwordx4 v[24:27], v[50:51], off offset:2064
	global_load_dwordx4 v[28:31], v[50:51], off offset:2048
.LBB0_926:
	v_add_f32_e32 v48, v48, v49
	v_fmamk_f32 v48, v48, 0x3a800000, v196
	v_cmp_gt_f32_e32 vcc, s35, v48
	v_mul_f32_e32 v49, 0x4b800000, v48
	v_and_b32_e32 v55, 0xffff0000, v44
	v_cndmask_b32_e32 v48, v48, v49, vcc
	v_rsq_f32_e32 v48, v48
	v_and_b32_e32 v53, 0xffff0000, v45
	v_lshlrev_b32_e32 v54, 16, v44
	v_lshlrev_b32_e32 v52, 16, v45
	v_mul_f32_e32 v49, 0x45800000, v48
	v_mul_f32_e32 v44, v55, v55
	v_mul_f32_e32 v45, v53, v53
	v_cndmask_b32_e32 v82, v48, v49, vcc
	v_and_b32_e32 v51, 0xffff0000, v46
	v_and_b32_e32 v49, 0xffff0000, v47
	v_fmac_f32_e32 v44, v54, v54
	v_fmac_f32_e32 v45, v52, v52
	v_lshlrev_b32_e32 v50, 16, v46
	v_lshlrev_b32_e32 v48, 16, v47
	v_add_f32_e32 v44, v44, v45
	v_mul_f32_e32 v45, v51, v51
	v_mul_f32_e32 v46, v49, v49
	v_fmac_f32_e32 v45, v50, v50
	v_fmac_f32_e32 v46, v48, v48
	v_add_f32_e32 v45, v45, v46
	v_add_f32_e32 v78, v44, v45
	v_and_b32_e32 v45, 0xffff0000, v40
	v_and_b32_e32 v47, 0xffff0000, v41
	v_lshlrev_b32_e32 v44, 16, v40
	v_lshlrev_b32_e32 v46, 16, v41
	v_mul_f32_e32 v79, v45, v45
	v_mul_f32_e32 v80, v47, v47
	v_lshlrev_b32_e32 v40, 16, v42
	v_and_b32_e32 v41, 0xffff0000, v42
	v_lshlrev_b32_e32 v42, 16, v43
	v_and_b32_e32 v43, 0xffff0000, v43
	v_fmac_f32_e32 v79, v44, v44
	v_fmac_f32_e32 v80, v46, v46
	v_add_f32_e32 v79, v79, v80
	v_mul_f32_e32 v80, v41, v41
	v_mul_f32_e32 v81, v43, v43
	v_fmac_f32_e32 v80, v40, v40
	v_fmac_f32_e32 v81, v42, v42
	v_add_f32_e32 v80, v80, v81
	v_add_f32_e32 v79, v79, v80
	v_add_f32_e32 v96, v78, v79
	v_pk_mul_f32 v[78:79], v[82:83], v[100:101] op_sel_hi:[0,1]
	v_pk_mul_f32 v[80:81], v[82:83], v[98:99] op_sel_hi:[0,1]
	v_pk_fma_f32 v[84:85], v[80:81], v[2:3], v[10:11]
	v_pk_fma_f32 v[86:87], v[78:79], v[0:1], v[8:9]
	v_pk_mul_f32 v[78:79], v[82:83], v[94:95] op_sel_hi:[0,1]
	v_pk_mul_f32 v[80:81], v[82:83], v[90:91] op_sel_hi:[0,1]
	v_pk_fma_f32 v[88:89], v[80:81], v[6:7], v[14:15]
	v_pk_fma_f32 v[90:91], v[78:79], v[4:5], v[12:13]
	v_cvt_pk_bf16_f32 v78, v86, v87
	v_cvt_pk_bf16_f32 v79, v84, v85
	v_cvt_pk_bf16_f32 v80, v90, v91
	v_cvt_pk_bf16_f32 v81, v88, v89
	v_lshl_add_u64 v[92:93], v[62:63], 0, s[46:47]
	global_store_dwordx4 v[92:93], v[78:81], off
	s_mul_hi_i32 s14, s42, 0x78787879
	s_lshr_b32 s28, s14, 31
	v_mov_b32_e32 v78, v113
	v_mov_b32_e32 v79, v113
	v_cvt_pk_fp8_f32 v78, v86, v87
	v_cvt_pk_fp8_f32 v79, v90, v91
	s_ashr_i32 s14, s14, 11
	s_add_i32 s14, s14, s28
	s_mul_i32 s28, s14, 0xffffef00
	s_add_i32 s28, s28, s42
	v_cvt_pk_fp8_f32 v78, v84, v85 op_sel:[0,0,1]
	v_cvt_pk_fp8_f32 v79, v88, v89 op_sel:[0,0,1]
	s_cmpk_gt_i32 s28, 0xff
	s_cselect_b32 s14, s14, 16
	s_lshl_b64 s[28:29], s[48:49], 10
	v_lshl_add_u64 v[80:81], v[68:69], 0, s[28:29]
	v_pk_mul_f32 v[72:73], v[82:83], v[72:73] op_sel_hi:[0,1]
	global_store_dwordx2 v[80:81], v[78:79], off
	v_pk_mul_f32 v[76:77], v[82:83], v[76:77] op_sel_hi:[0,1]
	s_waitcnt vmcnt(2)
	v_pk_fma_f32 v[78:79], v[72:73], v[16:17], v[28:29]
	v_pk_mul_f32 v[70:71], v[82:83], v[70:71] op_sel_hi:[0,1]
	v_pk_mul_f32 v[72:73], v[82:83], v[74:75] op_sel_hi:[0,1]
	v_pk_fma_f32 v[76:77], v[76:77], v[18:19], v[30:31]
	v_pk_fma_f32 v[74:75], v[72:73], v[22:23], v[26:27]
	v_pk_fma_f32 v[82:83], v[70:71], v[20:21], v[24:25]
	v_cvt_pk_bf16_f32 v70, v78, v79
	v_cvt_pk_bf16_f32 v71, v76, v77
	v_cvt_pk_bf16_f32 v72, v82, v83
	v_cvt_pk_bf16_f32 v73, v74, v75
	global_store_dwordx4 v[92:93], v[70:73], off offset:1024
	s_cmp_eq_u32 s14, s33
	s_mov_b64 s[64:65], 0xc00
	v_mov_b32_e32 v70, v113
	v_mov_b32_e32 v71, v113
	v_cvt_pk_fp8_f32 v70, v78, v79
	v_cvt_pk_fp8_f32 v71, v82, v83
	v_readlane_b32 s70, v255, 14
	s_mov_b32 s21, s20
	v_cvt_pk_fp8_f32 v70, v76, v77 op_sel:[0,0,1]
	v_cvt_pk_fp8_f32 v71, v74, v75 op_sel:[0,0,1]
	s_mov_b32 s71, s66
	global_store_dwordx2 v[80:81], v[70:71], off offset:512
	s_nop 1
	v_mov_b32_dpp v70, v96 quad_perm:[1,0,3,2] row_mask:0xf bank_mask:0xf
	s_waitcnt lgkmcnt(0)
	v_add_f32_e32 v70, v96, v70
	s_nop 1
	v_mov_b32_dpp v71, v70 quad_perm:[2,3,0,1] row_mask:0xf bank_mask:0xf
	s_waitcnt lgkmcnt(0)
	v_add_f32_e32 v70, v70, v71
	s_nop 1
	v_mov_b32_dpp v71, v70 row_half_mirror row_mask:0xf bank_mask:0xf
	s_waitcnt lgkmcnt(0)
	v_add_f32_e32 v70, v70, v71
	s_nop 1
	v_mov_b32_dpp v71, v70 row_mirror row_mask:0xf bank_mask:0xf
	s_waitcnt lgkmcnt(0)
	v_add_f32_e32 v70, v70, v71
	ds_swizzle_b32 v71, v70 offset:swizzle(SWAP,16)
	s_waitcnt lgkmcnt(0)
	v_add_f32_e32 v70, v70, v71
	v_mov_b32_e32 v71, v70
	s_nop 1
	v_permlane32_swap_b32_e32 v70, v71
	s_cbranch_scc1 .LBB0_928
	s_add_i32 s28, s14, s13
	s_mul_hi_i32 s29, s28, 0x6000
	s_mulk_i32 s28, 0x6000
	s_add_u32 s28, s60, s28
	s_addc_u32 s29, s63, s29
	v_lshl_add_u64 v[16:17], v[56:57], 2, s[28:29]
	v_add_co_u32_e32 v8, vcc, 0x4000, v16
	s_mov_b64 s[28:29], 0x4000
	s_nop 0
	v_addc_co_u32_e32 v9, vcc, 0, v17, vcc
	global_load_dwordx4 v[4:7], v[60:61], off offset:16
	global_load_dwordx4 v[0:3], v[60:61], off
	v_lshl_add_u64 v[28:29], v[16:17], 0, s[28:29]
	global_load_dwordx4 v[8:11], v[8:9], off
	s_nop 0
	global_load_dwordx4 v[12:15], v[28:29], off offset:16
	s_mov_b64 s[28:29], 0x3000
	v_lshl_add_u64 v[72:73], v[16:17], 0, s[28:29]
	s_movk_i32 s28, 0x3000
	s_mov_b32 s33, s14
	s_waitcnt vmcnt(1)
	v_pk_add_f32 v[8:9], v[8:9], 1.0 op_sel_hi:[1,0]
	s_nop 0
	v_pk_mul_f32 v[0:1], v[0:1], v[8:9]
	s_waitcnt vmcnt(0)
	v_pk_add_f32 v[8:9], v[14:15], 1.0 op_sel_hi:[1,0]
	v_pk_add_f32 v[10:11], v[10:11], 1.0 op_sel_hi:[1,0]
	v_pk_mul_f32 v[6:7], v[6:7], v[8:9]
	v_add_co_u32_e32 v8, vcc, s28, v16
	v_pk_mul_f32 v[2:3], v[2:3], v[10:11]
	v_pk_add_f32 v[10:11], v[12:13], 1.0 op_sel_hi:[1,0]
	v_addc_co_u32_e32 v9, vcc, 0, v17, vcc
	v_pk_mul_f32 v[4:5], v[4:5], v[10:11]
	global_load_dwordx4 v[8:11], v[8:9], off
	s_nop 0
	global_load_dwordx4 v[12:15], v[72:73], off offset:16
	global_load_dwordx4 v[20:23], v[60:61], off offset:2064
	global_load_dwordx4 v[16:19], v[60:61], off offset:2048
	global_load_dwordx4 v[24:27], v[28:29], off offset:2064
	s_nop 0
	global_load_dwordx4 v[28:31], v[28:29], off offset:2048
	s_waitcnt vmcnt(1)
	v_pk_add_f32 v[26:27], v[26:27], 1.0 op_sel_hi:[1,0]
	s_waitcnt vmcnt(0)
	v_pk_add_f32 v[30:31], v[30:31], 1.0 op_sel_hi:[1,0]
	v_pk_add_f32 v[28:29], v[28:29], 1.0 op_sel_hi:[1,0]
	v_pk_add_f32 v[24:25], v[24:25], 1.0 op_sel_hi:[1,0]
	v_pk_mul_f32 v[18:19], v[18:19], v[30:31]
	v_pk_mul_f32 v[16:17], v[16:17], v[28:29]
	v_pk_mul_f32 v[22:23], v[22:23], v[26:27]
	v_pk_mul_f32 v[20:21], v[20:21], v[24:25]
	global_load_dwordx4 v[24:27], v[72:73], off offset:2064
	global_load_dwordx4 v[28:31], v[72:73], off offset:2048
.LBB0_928:
	v_add_f32_e32 v70, v70, v71
	v_fmamk_f32 v70, v70, 0x3a800000, v196
	v_cmp_gt_f32_e32 vcc, s35, v70
	v_mul_f32_e32 v71, 0x4b800000, v70
	v_and_b32_e32 v79, 0xffff0000, v36
	v_cndmask_b32_e32 v70, v70, v71, vcc
	v_rsq_f32_e32 v70, v70
	v_and_b32_e32 v77, 0xffff0000, v37
	v_lshlrev_b32_e32 v78, 16, v36
	v_lshlrev_b32_e32 v76, 16, v37
	v_mul_f32_e32 v36, v79, v79
	v_mul_f32_e32 v37, v77, v77
	v_and_b32_e32 v75, 0xffff0000, v38
	v_and_b32_e32 v73, 0xffff0000, v39
	v_fmac_f32_e32 v36, v78, v78
	v_fmac_f32_e32 v37, v76, v76
	v_lshlrev_b32_e32 v74, 16, v38
	v_lshlrev_b32_e32 v72, 16, v39
	v_add_f32_e32 v36, v36, v37
	v_mul_f32_e32 v37, v75, v75
	v_mul_f32_e32 v38, v73, v73
	v_mul_f32_e32 v71, 0x45800000, v70
	v_fmac_f32_e32 v37, v74, v74
	v_fmac_f32_e32 v38, v72, v72
	v_cndmask_b32_e32 v80, v70, v71, vcc
	v_add_f32_e32 v37, v37, v38
	v_and_b32_e32 v71, 0xffff0000, v32
	v_and_b32_e32 v39, 0xffff0000, v33
	v_add_f32_e32 v81, v36, v37
	v_lshlrev_b32_e32 v70, 16, v32
	v_lshlrev_b32_e32 v38, 16, v33
	v_lshlrev_b32_e32 v36, 16, v34
	v_and_b32_e32 v37, 0xffff0000, v34
	v_lshlrev_b32_e32 v32, 16, v35
	v_and_b32_e32 v33, 0xffff0000, v35
	v_mul_f32_e32 v34, v71, v71
	v_mul_f32_e32 v35, v39, v39
	v_fmac_f32_e32 v34, v70, v70
	v_fmac_f32_e32 v35, v38, v38
	v_add_f32_e32 v34, v34, v35
	v_mul_f32_e32 v35, v37, v37
	v_mul_f32_e32 v82, v33, v33
	v_fmac_f32_e32 v35, v36, v36
	v_fmac_f32_e32 v82, v32, v32
	v_add_f32_e32 v35, v35, v82
	v_add_f32_e32 v34, v34, v35
	v_add_f32_e32 v81, v81, v34
	v_pk_mul_f32 v[34:35], v[80:81], v[54:55] op_sel_hi:[0,1]
	v_pk_mul_f32 v[52:53], v[80:81], v[52:53] op_sel_hi:[0,1]
	v_pk_mul_f32 v[50:51], v[80:81], v[50:51] op_sel_hi:[0,1]
	v_pk_mul_f32 v[48:49], v[80:81], v[48:49] op_sel_hi:[0,1]
	v_pk_fma_f32 v[52:53], v[52:53], v[2:3], v[10:11]
	v_pk_fma_f32 v[34:35], v[34:35], v[0:1], v[8:9]
	v_pk_fma_f32 v[54:55], v[48:49], v[6:7], v[14:15]
	v_pk_fma_f32 v[82:83], v[50:51], v[4:5], v[12:13]
	v_cvt_pk_bf16_f32 v48, v34, v35
	v_cvt_pk_bf16_f32 v49, v52, v53
	v_cvt_pk_bf16_f32 v50, v82, v83
	v_cvt_pk_bf16_f32 v51, v54, v55
	v_lshl_add_u64 v[84:85], v[62:63], 0, s[40:41]
	global_store_dwordx4 v[84:85], v[48:51], off
	s_mul_hi_i32 s14, s26, 0x78787879
	s_lshr_b32 s28, s14, 31
	v_mov_b32_e32 v48, v113
	v_mov_b32_e32 v49, v113
	v_cvt_pk_fp8_f32 v48, v34, v35
	v_cvt_pk_fp8_f32 v49, v82, v83
	s_ashr_i32 s14, s14, 11
	s_add_i32 s14, s14, s28
	s_mul_i32 s28, s14, 0xffffef00
	s_add_i32 s28, s28, s26
	v_cvt_pk_fp8_f32 v48, v52, v53 op_sel:[0,0,1]
	v_cvt_pk_fp8_f32 v49, v54, v55 op_sel:[0,0,1]
	s_cmpk_gt_i32 s28, 0xff
	s_cselect_b32 s14, s14, 16
	s_lshl_b64 s[28:29], s[42:43], 10
	v_lshl_add_u64 v[34:35], v[68:69], 0, s[28:29]
	v_pk_mul_f32 v[44:45], v[80:81], v[44:45] op_sel_hi:[0,1]
	v_pk_mul_f32 v[46:47], v[80:81], v[46:47] op_sel_hi:[0,1]
	v_pk_mul_f32 v[40:41], v[80:81], v[40:41] op_sel_hi:[0,1]
	v_pk_mul_f32 v[42:43], v[80:81], v[42:43] op_sel_hi:[0,1]
	global_store_dwordx2 v[34:35], v[48:49], off
	s_waitcnt vmcnt(2)
	v_pk_fma_f32 v[46:47], v[46:47], v[18:19], v[30:31]
	v_pk_fma_f32 v[44:45], v[44:45], v[16:17], v[28:29]
	v_pk_fma_f32 v[48:49], v[42:43], v[22:23], v[26:27]
	v_pk_fma_f32 v[50:51], v[40:41], v[20:21], v[24:25]
	v_cvt_pk_bf16_f32 v40, v44, v45
	v_cvt_pk_bf16_f32 v41, v46, v47
	v_cvt_pk_bf16_f32 v42, v50, v51
	v_cvt_pk_bf16_f32 v43, v48, v49
	global_store_dwordx4 v[84:85], v[40:43], off offset:1024
	s_cmp_eq_u32 s14, s33
	s_mov_b64 s[48:49], 0x80000
	v_mov_b32_e32 v40, v113
	v_mov_b32_e32 v41, v113
	v_cvt_pk_fp8_f32 v40, v44, v45
	v_cvt_pk_fp8_f32 v41, v50, v51
	v_cvt_pk_fp8_f32 v40, v46, v47 op_sel:[0,0,1]
	v_cvt_pk_fp8_f32 v41, v48, v49 op_sel:[0,0,1]
	global_store_dwordx2 v[34:35], v[40:41], off offset:512
	s_nop 1
	v_mov_b32_dpp v34, v81 quad_perm:[1,0,3,2] row_mask:0xf bank_mask:0xf
	s_waitcnt lgkmcnt(0)
	v_add_f32_e32 v34, v81, v34
	s_nop 1
	v_mov_b32_dpp v35, v34 quad_perm:[2,3,0,1] row_mask:0xf bank_mask:0xf
	s_waitcnt lgkmcnt(0)
	v_add_f32_e32 v34, v34, v35
	s_nop 1
	v_mov_b32_dpp v35, v34 row_half_mirror row_mask:0xf bank_mask:0xf
	s_waitcnt lgkmcnt(0)
	v_add_f32_e32 v34, v34, v35
	s_nop 1
	v_mov_b32_dpp v35, v34 row_mirror row_mask:0xf bank_mask:0xf
	s_waitcnt lgkmcnt(0)
	v_add_f32_e32 v34, v34, v35
	ds_swizzle_b32 v35, v34 offset:swizzle(SWAP,16)
	s_waitcnt lgkmcnt(0)
	v_add_f32_e32 v34, v34, v35
	v_mov_b32_e32 v35, v34
	s_nop 1
	v_permlane32_swap_b32_e32 v34, v35
	s_cbranch_scc1 .LBB0_921
	s_add_i32 s28, s14, s13
	s_mul_hi_i32 s29, s28, 0x6000
	s_mulk_i32 s28, 0x6000
	s_add_u32 s28, s60, s28
	s_addc_u32 s29, s63, s29
	v_lshl_add_u64 v[16:17], v[56:57], 2, s[28:29]
	v_add_co_u32_e32 v8, vcc, 0x4000, v16
	s_mov_b64 s[28:29], 0x4000
	s_nop 0
	v_addc_co_u32_e32 v9, vcc, 0, v17, vcc
	global_load_dwordx4 v[4:7], v[60:61], off offset:16
	global_load_dwordx4 v[0:3], v[60:61], off
	v_lshl_add_u64 v[28:29], v[16:17], 0, s[28:29]
	global_load_dwordx4 v[8:11], v[8:9], off
	s_nop 0
	global_load_dwordx4 v[12:15], v[28:29], off offset:16
	s_mov_b64 s[28:29], 0x3000
	v_lshl_add_u64 v[40:41], v[16:17], 0, s[28:29]
	s_movk_i32 s28, 0x3000
	s_waitcnt vmcnt(1)
	v_pk_add_f32 v[8:9], v[8:9], 1.0 op_sel_hi:[1,0]
	s_nop 0
	v_pk_mul_f32 v[0:1], v[0:1], v[8:9]
	s_waitcnt vmcnt(0)
	v_pk_add_f32 v[8:9], v[14:15], 1.0 op_sel_hi:[1,0]
	v_pk_add_f32 v[10:11], v[10:11], 1.0 op_sel_hi:[1,0]
	v_pk_mul_f32 v[6:7], v[6:7], v[8:9]
	v_add_co_u32_e32 v8, vcc, s28, v16
	v_pk_mul_f32 v[2:3], v[2:3], v[10:11]
	v_pk_add_f32 v[10:11], v[12:13], 1.0 op_sel_hi:[1,0]
	v_addc_co_u32_e32 v9, vcc, 0, v17, vcc
	v_pk_mul_f32 v[4:5], v[4:5], v[10:11]
	global_load_dwordx4 v[8:11], v[8:9], off
	s_nop 0
	global_load_dwordx4 v[12:15], v[40:41], off offset:16
	global_load_dwordx4 v[20:23], v[60:61], off offset:2064
	global_load_dwordx4 v[16:19], v[60:61], off offset:2048
	global_load_dwordx4 v[24:27], v[28:29], off offset:2064
	s_nop 0
	global_load_dwordx4 v[28:31], v[28:29], off offset:2048
	s_waitcnt vmcnt(1)
	v_pk_add_f32 v[26:27], v[26:27], 1.0 op_sel_hi:[1,0]
	s_waitcnt vmcnt(0)
	v_pk_add_f32 v[30:31], v[30:31], 1.0 op_sel_hi:[1,0]
	v_pk_add_f32 v[28:29], v[28:29], 1.0 op_sel_hi:[1,0]
	v_pk_add_f32 v[24:25], v[24:25], 1.0 op_sel_hi:[1,0]
	v_pk_mul_f32 v[18:19], v[18:19], v[30:31]
	v_pk_mul_f32 v[16:17], v[16:17], v[28:29]
	v_pk_mul_f32 v[22:23], v[22:23], v[26:27]
	v_pk_mul_f32 v[20:21], v[20:21], v[24:25]
	global_load_dwordx4 v[24:27], v[40:41], off offset:2064
	global_load_dwordx4 v[28:31], v[40:41], off offset:2048
	s_branch .LBB0_921
